# MoE XCD remap + software-pipelined final rmsnorm + hand-written f32 forward substitution (scalar FMAs, ring-buffered LDS reads) in the DeltaNet precompute
# speedup vs baseline: 1.0248x; 1.0145x over previous
.LBB0_338:
	s_andn2_b64 vcc, exec, s[0:1]
	s_cbranch_vccnz .LBB0_342
	v_and_b32_e32 v96, 31, v215
	v_lshrrev_b32_e32 v97, 5, v215
	v_and_b32_e32 v98, 15, v215
	v_lshrrev_b32_e32 v99, 4, v215
	v_mul_u32_u24_e32 v100, 0x2280, v97
	v_add_u32_e32 v100, 0x15c00, v100
	ds_read_b128 v[32:35], v100 offset:0
	ds_read_b128 v[36:39], v100 offset:16
	ds_read_b128 v[40:43], v100 offset:32
	ds_read_b128 v[44:47], v100 offset:48
	ds_read_b128 v[48:51], v100 offset:64
	ds_read_b128 v[52:55], v100 offset:80
	ds_read_b128 v[56:59], v100 offset:96
	ds_read_b128 v[60:63], v100 offset:112
	ds_read_b128 v[64:67], v100 offset:272
	ds_read_b128 v[68:71], v100 offset:288
	ds_read_b128 v[72:75], v100 offset:304
	ds_read_b128 v[76:79], v100 offset:320
	v_mov_b32_e32 v104, 1
	v_lshlrev_b32_e32 v105, v96, v104
	v_bfe_i32 v0, v105, 0, 1
	v_bfe_i32 v1, v105, 1, 1
	v_bfe_i32 v2, v105, 2, 1
	v_bfe_i32 v3, v105, 3, 1
	v_bfe_i32 v4, v105, 4, 1
	v_bfe_i32 v5, v105, 5, 1
	v_bfe_i32 v6, v105, 6, 1
	v_bfe_i32 v7, v105, 7, 1
	v_bfe_i32 v8, v105, 8, 1
	v_bfe_i32 v9, v105, 9, 1
	v_bfe_i32 v10, v105, 10, 1
	v_bfe_i32 v11, v105, 11, 1
	v_bfe_i32 v12, v105, 12, 1
	v_bfe_i32 v13, v105, 13, 1
	v_bfe_i32 v14, v105, 14, 1
	v_bfe_i32 v15, v105, 15, 1
	v_bfe_i32 v16, v105, 16, 1
	v_bfe_i32 v17, v105, 17, 1
	v_bfe_i32 v18, v105, 18, 1
	v_bfe_i32 v19, v105, 19, 1
	v_bfe_i32 v20, v105, 20, 1
	v_bfe_i32 v21, v105, 21, 1
	v_bfe_i32 v22, v105, 22, 1
	v_bfe_i32 v23, v105, 23, 1
	v_bfe_i32 v24, v105, 24, 1
	v_bfe_i32 v25, v105, 25, 1
	v_bfe_i32 v26, v105, 26, 1
	v_bfe_i32 v27, v105, 27, 1
	v_bfe_i32 v28, v105, 28, 1
	v_bfe_i32 v29, v105, 29, 1
	v_bfe_i32 v30, v105, 30, 1
	v_bfe_i32 v31, v105, 31, 1
	v_and_b32_e32 v0, 0x3f800000, v0
	v_and_b32_e32 v1, 0x3f800000, v1
	v_and_b32_e32 v2, 0x3f800000, v2
	v_and_b32_e32 v3, 0x3f800000, v3
	v_and_b32_e32 v4, 0x3f800000, v4
	v_and_b32_e32 v5, 0x3f800000, v5
	v_and_b32_e32 v6, 0x3f800000, v6
	v_and_b32_e32 v7, 0x3f800000, v7
	v_and_b32_e32 v8, 0x3f800000, v8
	v_and_b32_e32 v9, 0x3f800000, v9
	v_and_b32_e32 v10, 0x3f800000, v10
	v_and_b32_e32 v11, 0x3f800000, v11
	v_and_b32_e32 v12, 0x3f800000, v12
	v_and_b32_e32 v13, 0x3f800000, v13
	v_and_b32_e32 v14, 0x3f800000, v14
	v_and_b32_e32 v15, 0x3f800000, v15
	v_and_b32_e32 v16, 0x3f800000, v16
	v_and_b32_e32 v17, 0x3f800000, v17
	v_and_b32_e32 v18, 0x3f800000, v18
	v_and_b32_e32 v19, 0x3f800000, v19
	v_and_b32_e32 v20, 0x3f800000, v20
	v_and_b32_e32 v21, 0x3f800000, v21
	v_and_b32_e32 v22, 0x3f800000, v22
	v_and_b32_e32 v23, 0x3f800000, v23
	v_and_b32_e32 v24, 0x3f800000, v24
	v_and_b32_e32 v25, 0x3f800000, v25
	v_and_b32_e32 v26, 0x3f800000, v26
	v_and_b32_e32 v27, 0x3f800000, v27
	v_and_b32_e32 v28, 0x3f800000, v28
	v_and_b32_e32 v29, 0x3f800000, v29
	v_and_b32_e32 v30, 0x3f800000, v30
	v_and_b32_e32 v31, 0x3f800000, v31
	s_waitcnt lgkmcnt(11)
	v_fma_f32 v1, -v33, v0, v1
	v_fma_f32 v2, -v34, v0, v2
	v_fma_f32 v3, -v35, v0, v3
	s_waitcnt lgkmcnt(10)
	v_fma_f32 v4, -v36, v0, v4
	v_fma_f32 v5, -v37, v0, v5
	v_fma_f32 v6, -v38, v0, v6
	v_fma_f32 v7, -v39, v0, v7
	s_waitcnt lgkmcnt(9)
	v_fma_f32 v8, -v40, v0, v8
	v_fma_f32 v9, -v41, v0, v9
	v_fma_f32 v10, -v42, v0, v10
	v_fma_f32 v11, -v43, v0, v11
	s_waitcnt lgkmcnt(8)
	v_fma_f32 v12, -v44, v0, v12
	v_fma_f32 v13, -v45, v0, v13
	v_fma_f32 v14, -v46, v0, v14
	v_fma_f32 v15, -v47, v0, v15
	s_waitcnt lgkmcnt(7)
	v_fma_f32 v16, -v48, v0, v16
	v_fma_f32 v17, -v49, v0, v17
	v_fma_f32 v18, -v50, v0, v18
	v_fma_f32 v19, -v51, v0, v19
	s_waitcnt lgkmcnt(6)
	v_fma_f32 v20, -v52, v0, v20
	v_fma_f32 v21, -v53, v0, v21
	v_fma_f32 v22, -v54, v0, v22
	v_fma_f32 v23, -v55, v0, v23
	s_waitcnt lgkmcnt(5)
	v_fma_f32 v24, -v56, v0, v24
	v_fma_f32 v25, -v57, v0, v25
	v_fma_f32 v26, -v58, v0, v26
	v_fma_f32 v27, -v59, v0, v27
	s_waitcnt lgkmcnt(4)
	v_fma_f32 v28, -v60, v0, v28
	v_fma_f32 v29, -v61, v0, v29
	v_fma_f32 v30, -v62, v0, v30
	v_fma_f32 v31, -v63, v0, v31
	ds_read_b128 v[80:83], v100 offset:336
	ds_read_b128 v[84:87], v100 offset:352
	ds_read_b128 v[88:91], v100 offset:368
	ds_read_b128 v[92:95], v100 offset:384
	ds_read_b128 v[32:35], v100 offset:544
	ds_read_b128 v[36:39], v100 offset:560
	ds_read_b128 v[40:43], v100 offset:576
	ds_read_b128 v[44:47], v100 offset:592
	s_waitcnt lgkmcnt(11)
	v_fma_f32 v2, -v66, v1, v2
	v_fma_f32 v3, -v67, v1, v3
	s_waitcnt lgkmcnt(10)
	v_fma_f32 v4, -v68, v1, v4
	v_fma_f32 v5, -v69, v1, v5
	v_fma_f32 v6, -v70, v1, v6
	v_fma_f32 v7, -v71, v1, v7
	s_waitcnt lgkmcnt(9)
	v_fma_f32 v8, -v72, v1, v8
	v_fma_f32 v9, -v73, v1, v9
	v_fma_f32 v10, -v74, v1, v10
	v_fma_f32 v11, -v75, v1, v11
	s_waitcnt lgkmcnt(8)
	v_fma_f32 v12, -v76, v1, v12
	v_fma_f32 v13, -v77, v1, v13
	v_fma_f32 v14, -v78, v1, v14
	v_fma_f32 v15, -v79, v1, v15
	s_waitcnt lgkmcnt(7)
	v_fma_f32 v16, -v80, v1, v16
	v_fma_f32 v17, -v81, v1, v17
	v_fma_f32 v18, -v82, v1, v18
	v_fma_f32 v19, -v83, v1, v19
	s_waitcnt lgkmcnt(6)
	v_fma_f32 v20, -v84, v1, v20
	v_fma_f32 v21, -v85, v1, v21
	v_fma_f32 v22, -v86, v1, v22
	v_fma_f32 v23, -v87, v1, v23
	s_waitcnt lgkmcnt(5)
	v_fma_f32 v24, -v88, v1, v24
	v_fma_f32 v25, -v89, v1, v25
	v_fma_f32 v26, -v90, v1, v26
	v_fma_f32 v27, -v91, v1, v27
	s_waitcnt lgkmcnt(4)
	v_fma_f32 v28, -v92, v1, v28
	v_fma_f32 v29, -v93, v1, v29
	v_fma_f32 v30, -v94, v1, v30
	v_fma_f32 v31, -v95, v1, v31
	ds_read_b128 v[48:51], v100 offset:608
	ds_read_b128 v[52:55], v100 offset:624
	ds_read_b128 v[56:59], v100 offset:640
	ds_read_b128 v[60:63], v100 offset:656
	ds_read_b128 v[64:67], v100 offset:832
	ds_read_b128 v[68:71], v100 offset:848
	ds_read_b128 v[72:75], v100 offset:864
	ds_read_b128 v[76:79], v100 offset:880
	s_waitcnt lgkmcnt(11)
	v_fma_f32 v3, -v35, v2, v3
	s_waitcnt lgkmcnt(10)
	v_fma_f32 v4, -v36, v2, v4
	v_fma_f32 v5, -v37, v2, v5
	v_fma_f32 v6, -v38, v2, v6
	v_fma_f32 v7, -v39, v2, v7
	s_waitcnt lgkmcnt(9)
	v_fma_f32 v8, -v40, v2, v8
	v_fma_f32 v9, -v41, v2, v9
	v_fma_f32 v10, -v42, v2, v10
	v_fma_f32 v11, -v43, v2, v11
	s_waitcnt lgkmcnt(8)
	v_fma_f32 v12, -v44, v2, v12
	v_fma_f32 v13, -v45, v2, v13
	v_fma_f32 v14, -v46, v2, v14
	v_fma_f32 v15, -v47, v2, v15
	s_waitcnt lgkmcnt(7)
	v_fma_f32 v16, -v48, v2, v16
	v_fma_f32 v17, -v49, v2, v17
	v_fma_f32 v18, -v50, v2, v18
	v_fma_f32 v19, -v51, v2, v19
	s_waitcnt lgkmcnt(6)
	v_fma_f32 v20, -v52, v2, v20
	v_fma_f32 v21, -v53, v2, v21
	v_fma_f32 v22, -v54, v2, v22
	v_fma_f32 v23, -v55, v2, v23
	s_waitcnt lgkmcnt(5)
	v_fma_f32 v24, -v56, v2, v24
	v_fma_f32 v25, -v57, v2, v25
	v_fma_f32 v26, -v58, v2, v26
	v_fma_f32 v27, -v59, v2, v27
	s_waitcnt lgkmcnt(4)
	v_fma_f32 v28, -v60, v2, v28
	v_fma_f32 v29, -v61, v2, v29
	v_fma_f32 v30, -v62, v2, v30
	v_fma_f32 v31, -v63, v2, v31
	ds_read_b128 v[80:83], v100 offset:896
	ds_read_b128 v[84:87], v100 offset:912
	ds_read_b128 v[88:91], v100 offset:928
	ds_read_b128 v[92:95], v100 offset:1104
	ds_read_b128 v[32:35], v100 offset:1120
	ds_read_b128 v[36:39], v100 offset:1136
	ds_read_b128 v[40:43], v100 offset:1152
	ds_read_b128 v[44:47], v100 offset:1168
	s_waitcnt lgkmcnt(11)
	v_fma_f32 v4, -v64, v3, v4
	v_fma_f32 v5, -v65, v3, v5
	v_fma_f32 v6, -v66, v3, v6
	v_fma_f32 v7, -v67, v3, v7
	s_waitcnt lgkmcnt(10)
	v_fma_f32 v8, -v68, v3, v8
	v_fma_f32 v9, -v69, v3, v9
	v_fma_f32 v10, -v70, v3, v10
	v_fma_f32 v11, -v71, v3, v11
	s_waitcnt lgkmcnt(9)
	v_fma_f32 v12, -v72, v3, v12
	v_fma_f32 v13, -v73, v3, v13
	v_fma_f32 v14, -v74, v3, v14
	v_fma_f32 v15, -v75, v3, v15
	s_waitcnt lgkmcnt(8)
	v_fma_f32 v16, -v76, v3, v16
	v_fma_f32 v17, -v77, v3, v17
	v_fma_f32 v18, -v78, v3, v18
	v_fma_f32 v19, -v79, v3, v19
	s_waitcnt lgkmcnt(7)
	v_fma_f32 v20, -v80, v3, v20
	v_fma_f32 v21, -v81, v3, v21
	v_fma_f32 v22, -v82, v3, v22
	v_fma_f32 v23, -v83, v3, v23
	s_waitcnt lgkmcnt(6)
	v_fma_f32 v24, -v84, v3, v24
	v_fma_f32 v25, -v85, v3, v25
	v_fma_f32 v26, -v86, v3, v26
	v_fma_f32 v27, -v87, v3, v27
	s_waitcnt lgkmcnt(5)
	v_fma_f32 v28, -v88, v3, v28
	v_fma_f32 v29, -v89, v3, v29
	v_fma_f32 v30, -v90, v3, v30
	v_fma_f32 v31, -v91, v3, v31
	ds_read_b128 v[48:51], v100 offset:1184
	ds_read_b128 v[52:55], v100 offset:1200
	ds_read_b128 v[56:59], v100 offset:1376
	ds_read_b128 v[60:63], v100 offset:1392
	ds_read_b128 v[64:67], v100 offset:1408
	ds_read_b128 v[68:71], v100 offset:1424
	ds_read_b128 v[72:75], v100 offset:1440
	s_waitcnt lgkmcnt(11)
	v_fma_f32 v5, -v93, v4, v5
	v_fma_f32 v6, -v94, v4, v6
	v_fma_f32 v7, -v95, v4, v7
	s_waitcnt lgkmcnt(10)
	v_fma_f32 v8, -v32, v4, v8
	v_fma_f32 v9, -v33, v4, v9
	v_fma_f32 v10, -v34, v4, v10
	v_fma_f32 v11, -v35, v4, v11
	s_waitcnt lgkmcnt(9)
	v_fma_f32 v12, -v36, v4, v12
	v_fma_f32 v13, -v37, v4, v13
	v_fma_f32 v14, -v38, v4, v14
	v_fma_f32 v15, -v39, v4, v15
	s_waitcnt lgkmcnt(8)
	v_fma_f32 v16, -v40, v4, v16
	v_fma_f32 v17, -v41, v4, v17
	v_fma_f32 v18, -v42, v4, v18
	v_fma_f32 v19, -v43, v4, v19
	s_waitcnt lgkmcnt(7)
	v_fma_f32 v20, -v44, v4, v20
	v_fma_f32 v21, -v45, v4, v21
	v_fma_f32 v22, -v46, v4, v22
	v_fma_f32 v23, -v47, v4, v23
	s_waitcnt lgkmcnt(6)
	v_fma_f32 v24, -v48, v4, v24
	v_fma_f32 v25, -v49, v4, v25
	v_fma_f32 v26, -v50, v4, v26
	v_fma_f32 v27, -v51, v4, v27
	s_waitcnt lgkmcnt(5)
	v_fma_f32 v28, -v52, v4, v28
	v_fma_f32 v29, -v53, v4, v29
	v_fma_f32 v30, -v54, v4, v30
	v_fma_f32 v31, -v55, v4, v31
	ds_read_b128 v[76:79], v100 offset:1456
	ds_read_b128 v[80:83], v100 offset:1472
	ds_read_b128 v[84:87], v100 offset:1648
	ds_read_b128 v[88:91], v100 offset:1664
	ds_read_b128 v[92:95], v100 offset:1680
	ds_read_b128 v[32:35], v100 offset:1696
	ds_read_b128 v[36:39], v100 offset:1712
	s_waitcnt lgkmcnt(11)
	v_fma_f32 v6, -v58, v5, v6
	v_fma_f32 v7, -v59, v5, v7
	s_waitcnt lgkmcnt(10)
	v_fma_f32 v8, -v60, v5, v8
	v_fma_f32 v9, -v61, v5, v9
	v_fma_f32 v10, -v62, v5, v10
	v_fma_f32 v11, -v63, v5, v11
	s_waitcnt lgkmcnt(9)
	v_fma_f32 v12, -v64, v5, v12
	v_fma_f32 v13, -v65, v5, v13
	v_fma_f32 v14, -v66, v5, v14
	v_fma_f32 v15, -v67, v5, v15
	s_waitcnt lgkmcnt(8)
	v_fma_f32 v16, -v68, v5, v16
	v_fma_f32 v17, -v69, v5, v17
	v_fma_f32 v18, -v70, v5, v18
	v_fma_f32 v19, -v71, v5, v19
	s_waitcnt lgkmcnt(7)
	v_fma_f32 v20, -v72, v5, v20
	v_fma_f32 v21, -v73, v5, v21
	v_fma_f32 v22, -v74, v5, v22
	v_fma_f32 v23, -v75, v5, v23
	s_waitcnt lgkmcnt(6)
	v_fma_f32 v24, -v76, v5, v24
	v_fma_f32 v25, -v77, v5, v25
	v_fma_f32 v26, -v78, v5, v26
	v_fma_f32 v27, -v79, v5, v27
	s_waitcnt lgkmcnt(5)
	v_fma_f32 v28, -v80, v5, v28
	v_fma_f32 v29, -v81, v5, v29
	v_fma_f32 v30, -v82, v5, v30
	v_fma_f32 v31, -v83, v5, v31
	ds_read_b128 v[40:43], v100 offset:1728
	ds_read_b128 v[44:47], v100 offset:1744
	ds_read_b128 v[48:51], v100 offset:1936
	ds_read_b128 v[52:55], v100 offset:1952
	ds_read_b128 v[56:59], v100 offset:1968
	ds_read_b128 v[60:63], v100 offset:1984
	ds_read_b128 v[64:67], v100 offset:2000
	s_waitcnt lgkmcnt(11)
	v_fma_f32 v7, -v87, v6, v7
	s_waitcnt lgkmcnt(10)
	v_fma_f32 v8, -v88, v6, v8
	v_fma_f32 v9, -v89, v6, v9
	v_fma_f32 v10, -v90, v6, v10
	v_fma_f32 v11, -v91, v6, v11
	s_waitcnt lgkmcnt(9)
	v_fma_f32 v12, -v92, v6, v12
	v_fma_f32 v13, -v93, v6, v13
	v_fma_f32 v14, -v94, v6, v14
	v_fma_f32 v15, -v95, v6, v15
	s_waitcnt lgkmcnt(8)
	v_fma_f32 v16, -v32, v6, v16
	v_fma_f32 v17, -v33, v6, v17
	v_fma_f32 v18, -v34, v6, v18
	v_fma_f32 v19, -v35, v6, v19
	s_waitcnt lgkmcnt(7)
	v_fma_f32 v20, -v36, v6, v20
	v_fma_f32 v21, -v37, v6, v21
	v_fma_f32 v22, -v38, v6, v22
	v_fma_f32 v23, -v39, v6, v23
	s_waitcnt lgkmcnt(6)
	v_fma_f32 v24, -v40, v6, v24
	v_fma_f32 v25, -v41, v6, v25
	v_fma_f32 v26, -v42, v6, v26
	v_fma_f32 v27, -v43, v6, v27
	s_waitcnt lgkmcnt(5)
	v_fma_f32 v28, -v44, v6, v28
	v_fma_f32 v29, -v45, v6, v29
	v_fma_f32 v30, -v46, v6, v30
	v_fma_f32 v31, -v47, v6, v31
	ds_read_b128 v[68:71], v100 offset:2016
	ds_read_b128 v[72:75], v100 offset:2208
	ds_read_b128 v[76:79], v100 offset:2224
	ds_read_b128 v[80:83], v100 offset:2240
	ds_read_b128 v[84:87], v100 offset:2256
	ds_read_b128 v[88:91], v100 offset:2272
	ds_read_b128 v[92:95], v100 offset:2288
	s_waitcnt lgkmcnt(11)
	v_fma_f32 v8, -v48, v7, v8
	v_fma_f32 v9, -v49, v7, v9
	v_fma_f32 v10, -v50, v7, v10
	v_fma_f32 v11, -v51, v7, v11
	s_waitcnt lgkmcnt(10)
	v_fma_f32 v12, -v52, v7, v12
	v_fma_f32 v13, -v53, v7, v13
	v_fma_f32 v14, -v54, v7, v14
	v_fma_f32 v15, -v55, v7, v15
	s_waitcnt lgkmcnt(9)
	v_fma_f32 v16, -v56, v7, v16
	v_fma_f32 v17, -v57, v7, v17
	v_fma_f32 v18, -v58, v7, v18
	v_fma_f32 v19, -v59, v7, v19
	s_waitcnt lgkmcnt(8)
	v_fma_f32 v20, -v60, v7, v20
	v_fma_f32 v21, -v61, v7, v21
	v_fma_f32 v22, -v62, v7, v22
	v_fma_f32 v23, -v63, v7, v23
	s_waitcnt lgkmcnt(7)
	v_fma_f32 v24, -v64, v7, v24
	v_fma_f32 v25, -v65, v7, v25
	v_fma_f32 v26, -v66, v7, v26
	v_fma_f32 v27, -v67, v7, v27
	s_waitcnt lgkmcnt(6)
	v_fma_f32 v28, -v68, v7, v28
	v_fma_f32 v29, -v69, v7, v29
	v_fma_f32 v30, -v70, v7, v30
	v_fma_f32 v31, -v71, v7, v31
	ds_read_b128 v[32:35], v100 offset:2480
	ds_read_b128 v[36:39], v100 offset:2496
	ds_read_b128 v[40:43], v100 offset:2512
	ds_read_b128 v[44:47], v100 offset:2528
	ds_read_b128 v[48:51], v100 offset:2544
	ds_read_b128 v[52:55], v100 offset:2560
	s_waitcnt lgkmcnt(11)
	v_fma_f32 v9, -v73, v8, v9
	v_fma_f32 v10, -v74, v8, v10
	v_fma_f32 v11, -v75, v8, v11
	s_waitcnt lgkmcnt(10)
	v_fma_f32 v12, -v76, v8, v12
	v_fma_f32 v13, -v77, v8, v13
	v_fma_f32 v14, -v78, v8, v14
	v_fma_f32 v15, -v79, v8, v15
	s_waitcnt lgkmcnt(9)
	v_fma_f32 v16, -v80, v8, v16
	v_fma_f32 v17, -v81, v8, v17
	v_fma_f32 v18, -v82, v8, v18
	v_fma_f32 v19, -v83, v8, v19
	s_waitcnt lgkmcnt(8)
	v_fma_f32 v20, -v84, v8, v20
	v_fma_f32 v21, -v85, v8, v21
	v_fma_f32 v22, -v86, v8, v22
	v_fma_f32 v23, -v87, v8, v23
	s_waitcnt lgkmcnt(7)
	v_fma_f32 v24, -v88, v8, v24
	v_fma_f32 v25, -v89, v8, v25
	v_fma_f32 v26, -v90, v8, v26
	v_fma_f32 v27, -v91, v8, v27
	s_waitcnt lgkmcnt(6)
	v_fma_f32 v28, -v92, v8, v28
	v_fma_f32 v29, -v93, v8, v29
	v_fma_f32 v30, -v94, v8, v30
	v_fma_f32 v31, -v95, v8, v31
	ds_read_b128 v[56:59], v100 offset:2752
	ds_read_b128 v[60:63], v100 offset:2768
	ds_read_b128 v[64:67], v100 offset:2784
	ds_read_b128 v[68:71], v100 offset:2800
	ds_read_b128 v[72:75], v100 offset:2816
	ds_read_b128 v[76:79], v100 offset:2832
	s_waitcnt lgkmcnt(11)
	v_fma_f32 v10, -v34, v9, v10
	v_fma_f32 v11, -v35, v9, v11
	s_waitcnt lgkmcnt(10)
	v_fma_f32 v12, -v36, v9, v12
	v_fma_f32 v13, -v37, v9, v13
	v_fma_f32 v14, -v38, v9, v14
	v_fma_f32 v15, -v39, v9, v15
	s_waitcnt lgkmcnt(9)
	v_fma_f32 v16, -v40, v9, v16
	v_fma_f32 v17, -v41, v9, v17
	v_fma_f32 v18, -v42, v9, v18
	v_fma_f32 v19, -v43, v9, v19
	s_waitcnt lgkmcnt(8)
	v_fma_f32 v20, -v44, v9, v20
	v_fma_f32 v21, -v45, v9, v21
	v_fma_f32 v22, -v46, v9, v22
	v_fma_f32 v23, -v47, v9, v23
	s_waitcnt lgkmcnt(7)
	v_fma_f32 v24, -v48, v9, v24
	v_fma_f32 v25, -v49, v9, v25
	v_fma_f32 v26, -v50, v9, v26
	v_fma_f32 v27, -v51, v9, v27
	s_waitcnt lgkmcnt(6)
	v_fma_f32 v28, -v52, v9, v28
	v_fma_f32 v29, -v53, v9, v29
	v_fma_f32 v30, -v54, v9, v30
	v_fma_f32 v31, -v55, v9, v31
	ds_read_b128 v[80:83], v100 offset:3040
	ds_read_b128 v[84:87], v100 offset:3056
	ds_read_b128 v[88:91], v100 offset:3072
	ds_read_b128 v[92:95], v100 offset:3088
	ds_read_b128 v[32:35], v100 offset:3104
	ds_read_b128 v[36:39], v100 offset:3312
	s_waitcnt lgkmcnt(11)
	v_fma_f32 v11, -v59, v10, v11
	s_waitcnt lgkmcnt(10)
	v_fma_f32 v12, -v60, v10, v12
	v_fma_f32 v13, -v61, v10, v13
	v_fma_f32 v14, -v62, v10, v14
	v_fma_f32 v15, -v63, v10, v15
	s_waitcnt lgkmcnt(9)
	v_fma_f32 v16, -v64, v10, v16
	v_fma_f32 v17, -v65, v10, v17
	v_fma_f32 v18, -v66, v10, v18
	v_fma_f32 v19, -v67, v10, v19
	s_waitcnt lgkmcnt(8)
	v_fma_f32 v20, -v68, v10, v20
	v_fma_f32 v21, -v69, v10, v21
	v_fma_f32 v22, -v70, v10, v22
	v_fma_f32 v23, -v71, v10, v23
	s_waitcnt lgkmcnt(7)
	v_fma_f32 v24, -v72, v10, v24
	v_fma_f32 v25, -v73, v10, v25
	v_fma_f32 v26, -v74, v10, v26
	v_fma_f32 v27, -v75, v10, v27
	s_waitcnt lgkmcnt(6)
	v_fma_f32 v28, -v76, v10, v28
	v_fma_f32 v29, -v77, v10, v29
	v_fma_f32 v30, -v78, v10, v30
	v_fma_f32 v31, -v79, v10, v31
	ds_read_b128 v[40:43], v100 offset:3328
	ds_read_b128 v[44:47], v100 offset:3344
	ds_read_b128 v[48:51], v100 offset:3360
	ds_read_b128 v[52:55], v100 offset:3376
	ds_read_b128 v[56:59], v100 offset:3584
	ds_read_b128 v[60:63], v100 offset:3600
	s_waitcnt lgkmcnt(11)
	v_fma_f32 v12, -v80, v11, v12
	v_fma_f32 v13, -v81, v11, v13
	v_fma_f32 v14, -v82, v11, v14
	v_fma_f32 v15, -v83, v11, v15
	s_waitcnt lgkmcnt(10)
	v_fma_f32 v16, -v84, v11, v16
	v_fma_f32 v17, -v85, v11, v17
	v_fma_f32 v18, -v86, v11, v18
	v_fma_f32 v19, -v87, v11, v19
	s_waitcnt lgkmcnt(9)
	v_fma_f32 v20, -v88, v11, v20
	v_fma_f32 v21, -v89, v11, v21
	v_fma_f32 v22, -v90, v11, v22
	v_fma_f32 v23, -v91, v11, v23
	s_waitcnt lgkmcnt(8)
	v_fma_f32 v24, -v92, v11, v24
	v_fma_f32 v25, -v93, v11, v25
	v_fma_f32 v26, -v94, v11, v26
	v_fma_f32 v27, -v95, v11, v27
	s_waitcnt lgkmcnt(7)
	v_fma_f32 v28, -v32, v11, v28
	v_fma_f32 v29, -v33, v11, v29
	v_fma_f32 v30, -v34, v11, v30
	v_fma_f32 v31, -v35, v11, v31
	ds_read_b128 v[64:67], v100 offset:3616
	ds_read_b128 v[68:71], v100 offset:3632
	ds_read_b128 v[72:75], v100 offset:3648
	ds_read_b128 v[76:79], v100 offset:3856
	ds_read_b128 v[80:83], v100 offset:3872
	s_waitcnt lgkmcnt(11)
	v_fma_f32 v13, -v37, v12, v13
	v_fma_f32 v14, -v38, v12, v14
	v_fma_f32 v15, -v39, v12, v15
	s_waitcnt lgkmcnt(10)
	v_fma_f32 v16, -v40, v12, v16
	v_fma_f32 v17, -v41, v12, v17
	v_fma_f32 v18, -v42, v12, v18
	v_fma_f32 v19, -v43, v12, v19
	s_waitcnt lgkmcnt(9)
	v_fma_f32 v20, -v44, v12, v20
	v_fma_f32 v21, -v45, v12, v21
	v_fma_f32 v22, -v46, v12, v22
	v_fma_f32 v23, -v47, v12, v23
	s_waitcnt lgkmcnt(8)
	v_fma_f32 v24, -v48, v12, v24
	v_fma_f32 v25, -v49, v12, v25
	v_fma_f32 v26, -v50, v12, v26
	v_fma_f32 v27, -v51, v12, v27
	s_waitcnt lgkmcnt(7)
	v_fma_f32 v28, -v52, v12, v28
	v_fma_f32 v29, -v53, v12, v29
	v_fma_f32 v30, -v54, v12, v30
	v_fma_f32 v31, -v55, v12, v31
	ds_read_b128 v[84:87], v100 offset:3888
	ds_read_b128 v[88:91], v100 offset:3904
	ds_read_b128 v[92:95], v100 offset:3920
	ds_read_b128 v[32:35], v100 offset:4144
	ds_read_b128 v[36:39], v100 offset:4160
	s_waitcnt lgkmcnt(11)
	v_fma_f32 v14, -v58, v13, v14
	v_fma_f32 v15, -v59, v13, v15
	s_waitcnt lgkmcnt(10)
	v_fma_f32 v16, -v60, v13, v16
	v_fma_f32 v17, -v61, v13, v17
	v_fma_f32 v18, -v62, v13, v18
	v_fma_f32 v19, -v63, v13, v19
	s_waitcnt lgkmcnt(9)
	v_fma_f32 v20, -v64, v13, v20
	v_fma_f32 v21, -v65, v13, v21
	v_fma_f32 v22, -v66, v13, v22
	v_fma_f32 v23, -v67, v13, v23
	s_waitcnt lgkmcnt(8)
	v_fma_f32 v24, -v68, v13, v24
	v_fma_f32 v25, -v69, v13, v25
	v_fma_f32 v26, -v70, v13, v26
	v_fma_f32 v27, -v71, v13, v27
	s_waitcnt lgkmcnt(7)
	v_fma_f32 v28, -v72, v13, v28
	v_fma_f32 v29, -v73, v13, v29
	v_fma_f32 v30, -v74, v13, v30
	v_fma_f32 v31, -v75, v13, v31
	ds_read_b128 v[40:43], v100 offset:4176
	ds_read_b128 v[44:47], v100 offset:4192
	ds_read_b128 v[48:51], v100 offset:4416
	ds_read_b128 v[52:55], v100 offset:4432
	ds_read_b128 v[56:59], v100 offset:4448
	s_waitcnt lgkmcnt(11)
	v_fma_f32 v15, -v79, v14, v15
	s_waitcnt lgkmcnt(10)
	v_fma_f32 v16, -v80, v14, v16
	v_fma_f32 v17, -v81, v14, v17
	v_fma_f32 v18, -v82, v14, v18
	v_fma_f32 v19, -v83, v14, v19
	s_waitcnt lgkmcnt(9)
	v_fma_f32 v20, -v84, v14, v20
	v_fma_f32 v21, -v85, v14, v21
	v_fma_f32 v22, -v86, v14, v22
	v_fma_f32 v23, -v87, v14, v23
	s_waitcnt lgkmcnt(8)
	v_fma_f32 v24, -v88, v14, v24
	v_fma_f32 v25, -v89, v14, v25
	v_fma_f32 v26, -v90, v14, v26
	v_fma_f32 v27, -v91, v14, v27
	s_waitcnt lgkmcnt(7)
	v_fma_f32 v28, -v92, v14, v28
	v_fma_f32 v29, -v93, v14, v29
	v_fma_f32 v30, -v94, v14, v30
	v_fma_f32 v31, -v95, v14, v31
	ds_read_b128 v[60:63], v100 offset:4464
	ds_read_b128 v[64:67], v100 offset:4688
	ds_read_b128 v[68:71], v100 offset:4704
	ds_read_b128 v[72:75], v100 offset:4720
	ds_read_b128 v[76:79], v100 offset:4736
	s_waitcnt lgkmcnt(11)
	v_fma_f32 v16, -v32, v15, v16
	v_fma_f32 v17, -v33, v15, v17
	v_fma_f32 v18, -v34, v15, v18
	v_fma_f32 v19, -v35, v15, v19
	s_waitcnt lgkmcnt(10)
	v_fma_f32 v20, -v36, v15, v20
	v_fma_f32 v21, -v37, v15, v21
	v_fma_f32 v22, -v38, v15, v22
	v_fma_f32 v23, -v39, v15, v23
	s_waitcnt lgkmcnt(9)
	v_fma_f32 v24, -v40, v15, v24
	v_fma_f32 v25, -v41, v15, v25
	v_fma_f32 v26, -v42, v15, v26
	v_fma_f32 v27, -v43, v15, v27
	s_waitcnt lgkmcnt(8)
	v_fma_f32 v28, -v44, v15, v28
	v_fma_f32 v29, -v45, v15, v29
	v_fma_f32 v30, -v46, v15, v30
	v_fma_f32 v31, -v47, v15, v31
	ds_read_b128 v[80:83], v100 offset:4960
	ds_read_b128 v[84:87], v100 offset:4976
	ds_read_b128 v[88:91], v100 offset:4992
	ds_read_b128 v[92:95], v100 offset:5008
	s_waitcnt lgkmcnt(11)
	v_fma_f32 v17, -v49, v16, v17
	v_fma_f32 v18, -v50, v16, v18
	v_fma_f32 v19, -v51, v16, v19
	s_waitcnt lgkmcnt(10)
	v_fma_f32 v20, -v52, v16, v20
	v_fma_f32 v21, -v53, v16, v21
	v_fma_f32 v22, -v54, v16, v22
	v_fma_f32 v23, -v55, v16, v23
	s_waitcnt lgkmcnt(9)
	v_fma_f32 v24, -v56, v16, v24
	v_fma_f32 v25, -v57, v16, v25
	v_fma_f32 v26, -v58, v16, v26
	v_fma_f32 v27, -v59, v16, v27
	s_waitcnt lgkmcnt(8)
	v_fma_f32 v28, -v60, v16, v28
	v_fma_f32 v29, -v61, v16, v29
	v_fma_f32 v30, -v62, v16, v30
	v_fma_f32 v31, -v63, v16, v31
	ds_read_b128 v[32:35], v100 offset:5248
	ds_read_b128 v[36:39], v100 offset:5264
	ds_read_b128 v[40:43], v100 offset:5280
	ds_read_b128 v[44:47], v100 offset:5520
	s_waitcnt lgkmcnt(11)
	v_fma_f32 v18, -v66, v17, v18
	v_fma_f32 v19, -v67, v17, v19
	s_waitcnt lgkmcnt(10)
	v_fma_f32 v20, -v68, v17, v20
	v_fma_f32 v21, -v69, v17, v21
	v_fma_f32 v22, -v70, v17, v22
	v_fma_f32 v23, -v71, v17, v23
	s_waitcnt lgkmcnt(9)
	v_fma_f32 v24, -v72, v17, v24
	v_fma_f32 v25, -v73, v17, v25
	v_fma_f32 v26, -v74, v17, v26
	v_fma_f32 v27, -v75, v17, v27
	s_waitcnt lgkmcnt(8)
	v_fma_f32 v28, -v76, v17, v28
	v_fma_f32 v29, -v77, v17, v29
	v_fma_f32 v30, -v78, v17, v30
	v_fma_f32 v31, -v79, v17, v31
	ds_read_b128 v[48:51], v100 offset:5536
	ds_read_b128 v[52:55], v100 offset:5552
	ds_read_b128 v[56:59], v100 offset:5792
	ds_read_b128 v[60:63], v100 offset:5808
	s_waitcnt lgkmcnt(11)
	v_fma_f32 v19, -v83, v18, v19
	s_waitcnt lgkmcnt(10)
	v_fma_f32 v20, -v84, v18, v20
	v_fma_f32 v21, -v85, v18, v21
	v_fma_f32 v22, -v86, v18, v22
	v_fma_f32 v23, -v87, v18, v23
	s_waitcnt lgkmcnt(9)
	v_fma_f32 v24, -v88, v18, v24
	v_fma_f32 v25, -v89, v18, v25
	v_fma_f32 v26, -v90, v18, v26
	v_fma_f32 v27, -v91, v18, v27
	s_waitcnt lgkmcnt(8)
	v_fma_f32 v28, -v92, v18, v28
	v_fma_f32 v29, -v93, v18, v29
	v_fma_f32 v30, -v94, v18, v30
	v_fma_f32 v31, -v95, v18, v31
	ds_read_b128 v[64:67], v100 offset:5824
	ds_read_b128 v[68:71], v100 offset:6064
	ds_read_b128 v[72:75], v100 offset:6080
	ds_read_b128 v[76:79], v100 offset:6096
	s_waitcnt lgkmcnt(11)
	v_fma_f32 v20, -v32, v19, v20
	v_fma_f32 v21, -v33, v19, v21
	v_fma_f32 v22, -v34, v19, v22
	v_fma_f32 v23, -v35, v19, v23
	s_waitcnt lgkmcnt(10)
	v_fma_f32 v24, -v36, v19, v24
	v_fma_f32 v25, -v37, v19, v25
	v_fma_f32 v26, -v38, v19, v26
	v_fma_f32 v27, -v39, v19, v27
	s_waitcnt lgkmcnt(9)
	v_fma_f32 v28, -v40, v19, v28
	v_fma_f32 v29, -v41, v19, v29
	v_fma_f32 v30, -v42, v19, v30
	v_fma_f32 v31, -v43, v19, v31
	ds_read_b128 v[80:83], v100 offset:6352
	ds_read_b128 v[84:87], v100 offset:6368
	ds_read_b128 v[88:91], v100 offset:6624
	s_waitcnt lgkmcnt(11)
	v_fma_f32 v21, -v45, v20, v21
	v_fma_f32 v22, -v46, v20, v22
	v_fma_f32 v23, -v47, v20, v23
	s_waitcnt lgkmcnt(10)
	v_fma_f32 v24, -v48, v20, v24
	v_fma_f32 v25, -v49, v20, v25
	v_fma_f32 v26, -v50, v20, v26
	v_fma_f32 v27, -v51, v20, v27
	s_waitcnt lgkmcnt(9)
	v_fma_f32 v28, -v52, v20, v28
	v_fma_f32 v29, -v53, v20, v29
	v_fma_f32 v30, -v54, v20, v30
	v_fma_f32 v31, -v55, v20, v31
	ds_read_b128 v[92:95], v100 offset:6640
	ds_read_b128 v[32:35], v100 offset:6896
	ds_read_b128 v[36:39], v100 offset:6912
	s_waitcnt lgkmcnt(11)
	v_fma_f32 v22, -v58, v21, v22
	v_fma_f32 v23, -v59, v21, v23
	s_waitcnt lgkmcnt(10)
	v_fma_f32 v24, -v60, v21, v24
	v_fma_f32 v25, -v61, v21, v25
	v_fma_f32 v26, -v62, v21, v26
	v_fma_f32 v27, -v63, v21, v27
	s_waitcnt lgkmcnt(9)
	v_fma_f32 v28, -v64, v21, v28
	v_fma_f32 v29, -v65, v21, v29
	v_fma_f32 v30, -v66, v21, v30
	v_fma_f32 v31, -v67, v21, v31
	ds_read_b128 v[40:43], v100 offset:7168
	ds_read_b128 v[44:47], v100 offset:7184
	ds_read_b128 v[48:51], v100 offset:7456
	s_waitcnt lgkmcnt(11)
	v_fma_f32 v23, -v71, v22, v23
	s_waitcnt lgkmcnt(10)
	v_fma_f32 v24, -v72, v22, v24
	v_fma_f32 v25, -v73, v22, v25
	v_fma_f32 v26, -v74, v22, v26
	v_fma_f32 v27, -v75, v22, v27
	s_waitcnt lgkmcnt(9)
	v_fma_f32 v28, -v76, v22, v28
	v_fma_f32 v29, -v77, v22, v29
	v_fma_f32 v30, -v78, v22, v30
	v_fma_f32 v31, -v79, v22, v31
	ds_read_b128 v[52:55], v100 offset:7728
	ds_read_b128 v[56:59], v100 offset:8000
	ds_read_b128 v[60:63], v100 offset:8272
	s_waitcnt lgkmcnt(11)
	v_fma_f32 v24, -v80, v23, v24
	v_fma_f32 v25, -v81, v23, v25
	v_fma_f32 v26, -v82, v23, v26
	v_fma_f32 v27, -v83, v23, v27
	s_waitcnt lgkmcnt(10)
	v_fma_f32 v28, -v84, v23, v28
	v_fma_f32 v29, -v85, v23, v29
	v_fma_f32 v30, -v86, v23, v30
	v_fma_f32 v31, -v87, v23, v31
	s_waitcnt lgkmcnt(9)
	v_fma_f32 v25, -v89, v24, v25
	v_fma_f32 v26, -v90, v24, v26
	v_fma_f32 v27, -v91, v24, v27
	s_waitcnt lgkmcnt(8)
	v_fma_f32 v28, -v92, v24, v28
	v_fma_f32 v29, -v93, v24, v29
	v_fma_f32 v30, -v94, v24, v30
	v_fma_f32 v31, -v95, v24, v31
	s_waitcnt lgkmcnt(7)
	v_fma_f32 v26, -v34, v25, v26
	v_fma_f32 v27, -v35, v25, v27
	s_waitcnt lgkmcnt(6)
	v_fma_f32 v28, -v36, v25, v28
	v_fma_f32 v29, -v37, v25, v29
	v_fma_f32 v30, -v38, v25, v30
	v_fma_f32 v31, -v39, v25, v31
	s_waitcnt lgkmcnt(5)
	v_fma_f32 v27, -v43, v26, v27
	s_waitcnt lgkmcnt(4)
	v_fma_f32 v28, -v44, v26, v28
	v_fma_f32 v29, -v45, v26, v29
	v_fma_f32 v30, -v46, v26, v30
	v_fma_f32 v31, -v47, v26, v31
	s_waitcnt lgkmcnt(3)
	v_fma_f32 v28, -v48, v27, v28
	v_fma_f32 v29, -v49, v27, v29
	v_fma_f32 v30, -v50, v27, v30
	v_fma_f32 v31, -v51, v27, v31
	s_waitcnt lgkmcnt(2)
	v_fma_f32 v29, -v53, v28, v29
	v_fma_f32 v30, -v54, v28, v30
	v_fma_f32 v31, -v55, v28, v31
	s_waitcnt lgkmcnt(1)
	v_fma_f32 v30, -v58, v29, v30
	v_fma_f32 v31, -v59, v29, v31
	s_waitcnt lgkmcnt(0)
	v_fma_f32 v31, -v63, v30, v31
	v_mul_u32_u24_e32 v101, 0x1240, v97
	v_lshl_add_u32 v101, v96, 1, v101
	v_add_u32_e32 v101, 0x1a000, v101
	v_cvt_pk_bf16_f32 v110, v0, v1
	v_cvt_pk_bf16_f32 v111, v2, v3
	v_cvt_pk_bf16_f32 v112, v4, v5
	v_cvt_pk_bf16_f32 v113, v6, v7
	v_cvt_pk_bf16_f32 v114, v8, v9
	v_cvt_pk_bf16_f32 v115, v10, v11
	v_cvt_pk_bf16_f32 v116, v12, v13
	v_cvt_pk_bf16_f32 v117, v14, v15
	v_cvt_pk_bf16_f32 v118, v16, v17
	v_cvt_pk_bf16_f32 v119, v18, v19
	v_cvt_pk_bf16_f32 v120, v20, v21
	v_cvt_pk_bf16_f32 v121, v22, v23
	v_cvt_pk_bf16_f32 v122, v24, v25
	v_cvt_pk_bf16_f32 v123, v26, v27
	v_cvt_pk_bf16_f32 v124, v28, v29
	v_cvt_pk_bf16_f32 v125, v30, v31
	ds_write_b16 v101, v110 offset:0
	ds_write_b16_d16_hi v101, v110 offset:144
	ds_write_b16 v101, v111 offset:288
	ds_write_b16_d16_hi v101, v111 offset:432
	ds_write_b16 v101, v112 offset:576
	ds_write_b16_d16_hi v101, v112 offset:720
	ds_write_b16 v101, v113 offset:864
	ds_write_b16_d16_hi v101, v113 offset:1008
	ds_write_b16 v101, v114 offset:1152
	ds_write_b16_d16_hi v101, v114 offset:1296
	ds_write_b16 v101, v115 offset:1440
	ds_write_b16_d16_hi v101, v115 offset:1584
	ds_write_b16 v101, v116 offset:1728
	ds_write_b16_d16_hi v101, v116 offset:1872
	ds_write_b16 v101, v117 offset:2016
	ds_write_b16_d16_hi v101, v117 offset:2160
	ds_write_b16 v101, v118 offset:2304
	ds_write_b16_d16_hi v101, v118 offset:2448
	ds_write_b16 v101, v119 offset:2592
	ds_write_b16_d16_hi v101, v119 offset:2736
	ds_write_b16 v101, v120 offset:2880
	ds_write_b16_d16_hi v101, v120 offset:3024
	ds_write_b16 v101, v121 offset:3168
	ds_write_b16_d16_hi v101, v121 offset:3312
	ds_write_b16 v101, v122 offset:3456
	ds_write_b16_d16_hi v101, v122 offset:3600
	ds_write_b16 v101, v123 offset:3744
	ds_write_b16_d16_hi v101, v123 offset:3888
	ds_write_b16 v101, v124 offset:4032
	ds_write_b16_d16_hi v101, v124 offset:4176
	ds_write_b16 v101, v125 offset:4320
	ds_write_b16_d16_hi v101, v125 offset:4464
	v_lshrrev_b32_e32 v104, 2, v215
	v_mul_u32_u24_e32 v102, 0x90, v104
	v_and_b32_e32 v104, 3, v215
	v_lshl_add_u32 v102, v104, 4, v102
	v_add_u32_e32 v102, 0x1a040, v102
	v_mov_b32_e32 v106, 0
	v_mov_b32_e32 v107, 0
	v_mov_b32_e32 v108, 0
	v_mov_b32_e32 v109, 0
	ds_write_b128 v102, v[106:109]
	ds_write_b128 v102, v[106:109] offset:2304
	v_mul_u32_u24_e32 v103, 0x50, v96
	v_add_u32_e32 v103, 0x1d200, v103
	s_mov_b32 exec_lo, -1
	s_mov_b32 exec_hi, 0
	ds_write_b128 v103, v[110:113] offset:0
	ds_write_b128 v103, v[114:117] offset:16
	ds_write_b128 v103, v[118:121] offset:32
	ds_write_b128 v103, v[122:125] offset:48
	s_mov_b64 exec, -1
	v_mul_u32_u24_e32 v104, 0x50, v98
	v_lshl_add_u32 v126, v99, 4, v104
	v_add_u32_e32 v127, 0x1d200, v126
	v_add_u32_e32 v130, 0x1dc00, v126
	v_add_u32_e32 v126, 0x1c800, v126
	v_lshl_add_u32 v128, v99, 3, v104
	v_add_u32_e32 v128, 0x1dc00, v128
	v_mul_u32_u24_e32 v104, 0x90, v98
	v_lshl_add_u32 v129, v99, 4, v104
	v_add_u32_e32 v129, 0x1b240, v129
	v_mul_u32_u24_e32 v104, 0x240, v99
	v_lshl_add_u32 v131, v98, 1, v104
	v_add_u32_e32 v131, 0x1b200, v131
	s_waitcnt lgkmcnt(0)
	ds_read_b128 v[132:135], v126 offset:0
	ds_read_b128 v[136:139], v126 offset:1280
	ds_read_b128 v[144:147], v127 offset:0
	ds_read_b128 v[148:151], v127 offset:1280
	s_waitcnt lgkmcnt(0)
	v_mfma_f32_16x16x32_bf16 v[152:155], v[132:135], v[144:147], 0
	v_mfma_f32_16x16x32_bf16 v[156:159], v[132:135], v[148:151], 0
	v_mfma_f32_16x16x32_bf16 v[160:163], v[136:139], v[144:147], 0
	v_mfma_f32_16x16x32_bf16 v[164:167], v[136:139], v[148:151], 0
	s_nop 7
	v_cvt_pk_bf16_f32 v168, v152, v153
	v_cvt_pk_bf16_f32 v169, v154, v155
	ds_write_b64 v128, v[168:169] offset:0
	v_cvt_pk_bf16_f32 v170, v156, v157
	v_cvt_pk_bf16_f32 v171, v158, v159
	ds_write_b64 v128, v[170:171] offset:1280
	v_cvt_pk_bf16_f32 v168, v160, v161
	v_cvt_pk_bf16_f32 v169, v162, v163
	ds_write_b64 v128, v[168:169] offset:32
	v_cvt_pk_bf16_f32 v170, v164, v165
	v_cvt_pk_bf16_f32 v171, v166, v167
	ds_write_b64 v128, v[170:171] offset:1312
	s_waitcnt lgkmcnt(0)
	ds_read_b128 v[132:135], v129 offset:0
	ds_read_b128 v[136:139], v129 offset:2304
	ds_read_b128 v[144:147], v130 offset:0
	ds_read_b128 v[148:151], v130 offset:1280
	s_waitcnt lgkmcnt(0)
	v_mfma_f32_16x16x32_bf16 v[152:155], v[132:135], v[144:147], 0
	v_mfma_f32_16x16x32_bf16 v[156:159], v[132:135], v[148:151], 0
	v_mfma_f32_16x16x32_bf16 v[160:163], v[136:139], v[144:147], 0
	v_mfma_f32_16x16x32_bf16 v[164:167], v[136:139], v[148:151], 0
	s_nop 7
	v_cvt_pk_bf16_f32 v152, -v152, v152
	v_cvt_pk_bf16_f32 v153, -v153, v153
	v_cvt_pk_bf16_f32 v154, -v154, v154
	v_cvt_pk_bf16_f32 v155, -v155, v155
	ds_write_b16 v131, v152 offset:0
	ds_write_b16 v131, v153 offset:144
	ds_write_b16 v131, v154 offset:288
	ds_write_b16 v131, v155 offset:432
	v_cvt_pk_bf16_f32 v156, -v156, v156
	v_cvt_pk_bf16_f32 v157, -v157, v157
	v_cvt_pk_bf16_f32 v158, -v158, v158
	v_cvt_pk_bf16_f32 v159, -v159, v159
	ds_write_b16 v131, v156 offset:32
	ds_write_b16 v131, v157 offset:176
	ds_write_b16 v131, v158 offset:320
	ds_write_b16 v131, v159 offset:464
	v_cvt_pk_bf16_f32 v160, -v160, v160
	v_cvt_pk_bf16_f32 v161, -v161, v161
	v_cvt_pk_bf16_f32 v162, -v162, v162
	v_cvt_pk_bf16_f32 v163, -v163, v163
	ds_write_b16 v131, v160 offset:2304
	ds_write_b16 v131, v161 offset:2448
	ds_write_b16 v131, v162 offset:2592
	ds_write_b16 v131, v163 offset:2736
	v_cvt_pk_bf16_f32 v164, -v164, v164
	v_cvt_pk_bf16_f32 v165, -v165, v165
	v_cvt_pk_bf16_f32 v166, -v166, v166
	v_cvt_pk_bf16_f32 v167, -v167, v167
	ds_write_b16 v131, v164 offset:2336
	ds_write_b16 v131, v165 offset:2480
	ds_write_b16 v131, v166 offset:2624
	ds_write_b16 v131, v167 offset:2768

.LBB0_1166:
	s_cmp_lt_i32 s90, 13
	s_cselect_b64 s[4:5], -1, 0
	s_and_b64 s[2:3], s[4:5], s[2:3]
	s_andn2_b64 vcc, exec, s[2:3]
	s_cbranch_vccnz .LBB0_1174
	s_waitcnt vmcnt(0)
	s_mov_b64 exec, -1
	s_add_u32 s4, s88, 0x12400000
	s_addc_u32 s5, s89, 0
	s_add_u32 s6, s88, 0x1000
	s_addc_u32 s7, s89, 0
	s_mov_b32 s11, 0x800000
	v_and_b32_e32 v8, 0x7f, v236
	v_lshrrev_b32_e32 v9, 7, v236
	v_lshl_add_u32 v9, s30, 2, v9
	v_lshlrev_b32_e32 v14, 5, v8
	global_load_dwordx4 v[0:3], v14, s[84:85] offset:16
	global_load_dwordx4 v[4:7], v14, s[84:85]
	v_lshlrev_b32_e32 v10, 4, v8
	v_lshl_add_u32 v10, v9, 11, v10
	v_lshlrev_b32_e32 v11, 2, v9
	v_lshl_add_u32 v12, v9, 12, v14
	v_mov_b32_e32 v13, 0x358637bd
	global_load_dword v20, v11, s[6:7]
	global_load_dwordx4 v[16:19], v10, s[4:5] nt
	v_add_u32_e32 v194, 0x1000, v11
	v_add_u32_e32 v195, 0x200000, v10
	global_load_dword v26, v194, s[6:7]
	global_load_dwordx4 v[22:25], v195, s[4:5] nt
	v_add_u32_e32 v196, 0x2000, v11
	v_add_u32_e32 v197, 0x400000, v10
	global_load_dword v32, v196, s[6:7]
	global_load_dwordx4 v[28:31], v197, s[4:5] nt
	v_add_u32_e32 v198, 0x3000, v11
	v_add_u32_e32 v199, 0x600000, v10
	global_load_dword v38, v198, s[6:7]
	global_load_dwordx4 v[34:37], v199, s[4:5] nt
	v_add_u32_e32 v200, 0x4000, v11
	v_add_u32_e32 v201, 0x800000, v10
	global_load_dword v44, v200, s[6:7]
	global_load_dwordx4 v[40:43], v201, s[4:5] nt
	v_add_u32_e32 v202, 0x5000, v11
	v_add_u32_e32 v203, 0xa00000, v10
	global_load_dword v50, v202, s[6:7]
	global_load_dwordx4 v[46:49], v203, s[4:5] nt
	v_add_u32_e32 v204, 0x6000, v11
	v_add_u32_e32 v205, 0xc00000, v10
	global_load_dword v56, v204, s[6:7]
	global_load_dwordx4 v[52:55], v205, s[4:5] nt
	v_add_u32_e32 v206, 0x7000, v11
	v_add_u32_e32 v207, 0xe00000, v10
	global_load_dword v62, v206, s[6:7]
	global_load_dwordx4 v[58:61], v207, s[4:5] nt
	v_add_u32_e32 v208, 0x8000, v11
	v_add_u32_e32 v209, 0x1000000, v10
	global_load_dword v68, v208, s[6:7]
	global_load_dwordx4 v[64:67], v209, s[4:5] nt
	s_waitcnt vmcnt(16)
	v_fmamk_f32 v100, v20, 0x3a800000, v13
	v_mul_f32_e32 v101, 0x4b800000, v100
	v_cmp_gt_f32_e32 vcc, s11, v100
	v_lshlrev_b32_e32 v102, 16, v16
	v_and_b32_e32 v103, 0xffff0000, v16
	v_cndmask_b32_e32 v100, v100, v101, vcc
	v_rsq_f32_e32 v100, v100
	v_lshlrev_b32_e32 v104, 16, v17
	v_mul_f32_e32 v101, 0x45800000, v100
	v_and_b32_e32 v105, 0xffff0000, v17
	v_cndmask_b32_e32 v101, v100, v101, vcc
	v_lshlrev_b32_e32 v106, 16, v18
	v_and_b32_e32 v107, 0xffff0000, v18
	v_lshlrev_b32_e32 v108, 16, v19
	v_and_b32_e32 v109, 0xffff0000, v19
	v_mul_f32_e32 v102, v101, v102
	v_mul_f32_e32 v103, v101, v103
	v_mul_f32_e32 v104, v101, v104
	v_mul_f32_e32 v105, v101, v105
	v_mul_f32_e32 v106, v101, v106
	v_mul_f32_e32 v107, v101, v107
	v_mul_f32_e32 v108, v101, v108
	v_mul_f32_e32 v109, v101, v109
	v_mul_f32_e32 v102, v4, v102
	v_mul_f32_e32 v103, v5, v103
	v_mul_f32_e32 v104, v6, v104
	v_mul_f32_e32 v105, v7, v105
	v_mul_f32_e32 v106, v0, v106
	v_mul_f32_e32 v107, v1, v107
	v_mul_f32_e32 v108, v2, v108
	v_mul_f32_e32 v109, v3, v109
	global_store_dwordx4 v12, v[102:105], s[86:87] nt
	global_store_dwordx4 v12, v[106:109], s[86:87] offset:16 nt
	v_add_u32_e32 v210, 0x9000, v11
	v_add_u32_e32 v211, 0x1200000, v10
	global_load_dword v20, v210, s[6:7]
	global_load_dwordx4 v[16:19], v211, s[4:5] nt
	s_waitcnt vmcnt(18)
	v_fmamk_f32 v110, v26, 0x3a800000, v13
	v_mul_f32_e32 v111, 0x4b800000, v110
	v_cmp_gt_f32_e32 vcc, s11, v110
	v_lshlrev_b32_e32 v112, 16, v22
	v_and_b32_e32 v113, 0xffff0000, v22
	v_cndmask_b32_e32 v110, v110, v111, vcc
	v_rsq_f32_e32 v110, v110
	v_lshlrev_b32_e32 v114, 16, v23
	v_mul_f32_e32 v111, 0x45800000, v110
	v_and_b32_e32 v115, 0xffff0000, v23
	v_cndmask_b32_e32 v111, v110, v111, vcc
	v_lshlrev_b32_e32 v116, 16, v24
	v_and_b32_e32 v117, 0xffff0000, v24
	v_lshlrev_b32_e32 v118, 16, v25
	v_and_b32_e32 v119, 0xffff0000, v25
	v_mul_f32_e32 v112, v111, v112
	v_mul_f32_e32 v113, v111, v113
	v_mul_f32_e32 v114, v111, v114
	v_mul_f32_e32 v115, v111, v115
	v_mul_f32_e32 v116, v111, v116
	v_mul_f32_e32 v117, v111, v117
	v_mul_f32_e32 v118, v111, v118
	v_mul_f32_e32 v119, v111, v119
	v_mul_f32_e32 v112, v4, v112
	v_mul_f32_e32 v113, v5, v113
	v_mul_f32_e32 v114, v6, v114
	v_mul_f32_e32 v115, v7, v115
	v_mul_f32_e32 v116, v0, v116
	v_mul_f32_e32 v117, v1, v117
	v_mul_f32_e32 v118, v2, v118
	v_mul_f32_e32 v119, v3, v119
	v_add_u32_e32 v212, 0x400000, v12
	global_store_dwordx4 v212, v[112:115], s[86:87] nt
	global_store_dwordx4 v212, v[116:119], s[86:87] offset:16 nt
	v_add_u32_e32 v213, 0xa000, v11
	v_add_u32_e32 v214, 0x1400000, v10
	global_load_dword v26, v213, s[6:7]
	global_load_dwordx4 v[22:25], v214, s[4:5] nt
	s_waitcnt vmcnt(20)
	v_fmamk_f32 v100, v32, 0x3a800000, v13
	v_mul_f32_e32 v101, 0x4b800000, v100
	v_cmp_gt_f32_e32 vcc, s11, v100
	v_lshlrev_b32_e32 v102, 16, v28
	v_and_b32_e32 v103, 0xffff0000, v28
	v_cndmask_b32_e32 v100, v100, v101, vcc
	v_rsq_f32_e32 v100, v100
	v_lshlrev_b32_e32 v104, 16, v29
	v_mul_f32_e32 v101, 0x45800000, v100
	v_and_b32_e32 v105, 0xffff0000, v29
	v_cndmask_b32_e32 v101, v100, v101, vcc
	v_lshlrev_b32_e32 v106, 16, v30
	v_and_b32_e32 v107, 0xffff0000, v30
	v_lshlrev_b32_e32 v108, 16, v31
	v_and_b32_e32 v109, 0xffff0000, v31
	v_mul_f32_e32 v102, v101, v102
	v_mul_f32_e32 v103, v101, v103
	v_mul_f32_e32 v104, v101, v104
	v_mul_f32_e32 v105, v101, v105
	v_mul_f32_e32 v106, v101, v106
	v_mul_f32_e32 v107, v101, v107
	v_mul_f32_e32 v108, v101, v108
	v_mul_f32_e32 v109, v101, v109
	v_mul_f32_e32 v102, v4, v102
	v_mul_f32_e32 v103, v5, v103
	v_mul_f32_e32 v104, v6, v104
	v_mul_f32_e32 v105, v7, v105
	v_mul_f32_e32 v106, v0, v106
	v_mul_f32_e32 v107, v1, v107
	v_mul_f32_e32 v108, v2, v108
	v_mul_f32_e32 v109, v3, v109
	v_add_u32_e32 v215, 0x800000, v12
	global_store_dwordx4 v215, v[102:105], s[86:87] nt
	global_store_dwordx4 v215, v[106:109], s[86:87] offset:16 nt
	v_add_u32_e32 v192, 0xb000, v11
	v_add_u32_e32 v193, 0x1600000, v10
	global_load_dword v32, v192, s[6:7]
	global_load_dwordx4 v[28:31], v193, s[4:5] nt
	s_waitcnt vmcnt(22)
	v_fmamk_f32 v110, v38, 0x3a800000, v13
	v_mul_f32_e32 v111, 0x4b800000, v110
	v_cmp_gt_f32_e32 vcc, s11, v110
	v_lshlrev_b32_e32 v112, 16, v34
	v_and_b32_e32 v113, 0xffff0000, v34
	v_cndmask_b32_e32 v110, v110, v111, vcc
	v_rsq_f32_e32 v110, v110
	v_lshlrev_b32_e32 v114, 16, v35
	v_mul_f32_e32 v111, 0x45800000, v110
	v_and_b32_e32 v115, 0xffff0000, v35
	v_cndmask_b32_e32 v111, v110, v111, vcc
	v_lshlrev_b32_e32 v116, 16, v36
	v_and_b32_e32 v117, 0xffff0000, v36
	v_lshlrev_b32_e32 v118, 16, v37
	v_and_b32_e32 v119, 0xffff0000, v37
	v_mul_f32_e32 v112, v111, v112
	v_mul_f32_e32 v113, v111, v113
	v_mul_f32_e32 v114, v111, v114
	v_mul_f32_e32 v115, v111, v115
	v_mul_f32_e32 v116, v111, v116
	v_mul_f32_e32 v117, v111, v117
	v_mul_f32_e32 v118, v111, v118
	v_mul_f32_e32 v119, v111, v119
	v_mul_f32_e32 v112, v4, v112
	v_mul_f32_e32 v113, v5, v113
	v_mul_f32_e32 v114, v6, v114
	v_mul_f32_e32 v115, v7, v115
	v_mul_f32_e32 v116, v0, v116
	v_mul_f32_e32 v117, v1, v117
	v_mul_f32_e32 v118, v2, v118
	v_mul_f32_e32 v119, v3, v119
	v_add_u32_e32 v194, 0xc00000, v12
	global_store_dwordx4 v194, v[112:115], s[86:87] nt
	global_store_dwordx4 v194, v[116:119], s[86:87] offset:16 nt
	v_add_u32_e32 v195, 0xc000, v11
	v_add_u32_e32 v196, 0x1800000, v10
	global_load_dword v38, v195, s[6:7]
	global_load_dwordx4 v[34:37], v196, s[4:5] nt
	s_waitcnt vmcnt(24)
	v_fmamk_f32 v100, v44, 0x3a800000, v13
	v_mul_f32_e32 v101, 0x4b800000, v100
	v_cmp_gt_f32_e32 vcc, s11, v100
	v_lshlrev_b32_e32 v102, 16, v40
	v_and_b32_e32 v103, 0xffff0000, v40
	v_cndmask_b32_e32 v100, v100, v101, vcc
	v_rsq_f32_e32 v100, v100
	v_lshlrev_b32_e32 v104, 16, v41
	v_mul_f32_e32 v101, 0x45800000, v100
	v_and_b32_e32 v105, 0xffff0000, v41
	v_cndmask_b32_e32 v101, v100, v101, vcc
	v_lshlrev_b32_e32 v106, 16, v42
	v_and_b32_e32 v107, 0xffff0000, v42
	v_lshlrev_b32_e32 v108, 16, v43
	v_and_b32_e32 v109, 0xffff0000, v43
	v_mul_f32_e32 v102, v101, v102
	v_mul_f32_e32 v103, v101, v103
	v_mul_f32_e32 v104, v101, v104
	v_mul_f32_e32 v105, v101, v105
	v_mul_f32_e32 v106, v101, v106
	v_mul_f32_e32 v107, v101, v107
	v_mul_f32_e32 v108, v101, v108
	v_mul_f32_e32 v109, v101, v109
	v_mul_f32_e32 v102, v4, v102
	v_mul_f32_e32 v103, v5, v103
	v_mul_f32_e32 v104, v6, v104
	v_mul_f32_e32 v105, v7, v105
	v_mul_f32_e32 v106, v0, v106
	v_mul_f32_e32 v107, v1, v107
	v_mul_f32_e32 v108, v2, v108
	v_mul_f32_e32 v109, v3, v109
	v_add_u32_e32 v197, 0x1000000, v12
	global_store_dwordx4 v197, v[102:105], s[86:87] nt
	global_store_dwordx4 v197, v[106:109], s[86:87] offset:16 nt
	v_add_u32_e32 v198, 0xd000, v11
	v_add_u32_e32 v199, 0x1a00000, v10
	global_load_dword v44, v198, s[6:7]
	global_load_dwordx4 v[40:43], v199, s[4:5] nt
	s_waitcnt vmcnt(26)
	v_fmamk_f32 v110, v50, 0x3a800000, v13
	v_mul_f32_e32 v111, 0x4b800000, v110
	v_cmp_gt_f32_e32 vcc, s11, v110
	v_lshlrev_b32_e32 v112, 16, v46
	v_and_b32_e32 v113, 0xffff0000, v46
	v_cndmask_b32_e32 v110, v110, v111, vcc
	v_rsq_f32_e32 v110, v110
	v_lshlrev_b32_e32 v114, 16, v47
	v_mul_f32_e32 v111, 0x45800000, v110
	v_and_b32_e32 v115, 0xffff0000, v47
	v_cndmask_b32_e32 v111, v110, v111, vcc
	v_lshlrev_b32_e32 v116, 16, v48
	v_and_b32_e32 v117, 0xffff0000, v48
	v_lshlrev_b32_e32 v118, 16, v49
	v_and_b32_e32 v119, 0xffff0000, v49
	v_mul_f32_e32 v112, v111, v112
	v_mul_f32_e32 v113, v111, v113
	v_mul_f32_e32 v114, v111, v114
	v_mul_f32_e32 v115, v111, v115
	v_mul_f32_e32 v116, v111, v116
	v_mul_f32_e32 v117, v111, v117
	v_mul_f32_e32 v118, v111, v118
	v_mul_f32_e32 v119, v111, v119
	v_mul_f32_e32 v112, v4, v112
	v_mul_f32_e32 v113, v5, v113
	v_mul_f32_e32 v114, v6, v114
	v_mul_f32_e32 v115, v7, v115
	v_mul_f32_e32 v116, v0, v116
	v_mul_f32_e32 v117, v1, v117
	v_mul_f32_e32 v118, v2, v118
	v_mul_f32_e32 v119, v3, v119
	v_add_u32_e32 v200, 0x1400000, v12
	global_store_dwordx4 v200, v[112:115], s[86:87] nt
	global_store_dwordx4 v200, v[116:119], s[86:87] offset:16 nt
	v_add_u32_e32 v201, 0xe000, v11
	v_add_u32_e32 v202, 0x1c00000, v10
	global_load_dword v50, v201, s[6:7]
	global_load_dwordx4 v[46:49], v202, s[4:5] nt
	s_waitcnt vmcnt(28)
	v_fmamk_f32 v100, v56, 0x3a800000, v13
	v_mul_f32_e32 v101, 0x4b800000, v100
	v_cmp_gt_f32_e32 vcc, s11, v100
	v_lshlrev_b32_e32 v102, 16, v52
	v_and_b32_e32 v103, 0xffff0000, v52
	v_cndmask_b32_e32 v100, v100, v101, vcc
	v_rsq_f32_e32 v100, v100
	v_lshlrev_b32_e32 v104, 16, v53
	v_mul_f32_e32 v101, 0x45800000, v100
	v_and_b32_e32 v105, 0xffff0000, v53
	v_cndmask_b32_e32 v101, v100, v101, vcc
	v_lshlrev_b32_e32 v106, 16, v54
	v_and_b32_e32 v107, 0xffff0000, v54
	v_lshlrev_b32_e32 v108, 16, v55
	v_and_b32_e32 v109, 0xffff0000, v55
	v_mul_f32_e32 v102, v101, v102
	v_mul_f32_e32 v103, v101, v103
	v_mul_f32_e32 v104, v101, v104
	v_mul_f32_e32 v105, v101, v105
	v_mul_f32_e32 v106, v101, v106
	v_mul_f32_e32 v107, v101, v107
	v_mul_f32_e32 v108, v101, v108
	v_mul_f32_e32 v109, v101, v109
	v_mul_f32_e32 v102, v4, v102
	v_mul_f32_e32 v103, v5, v103
	v_mul_f32_e32 v104, v6, v104
	v_mul_f32_e32 v105, v7, v105
	v_mul_f32_e32 v106, v0, v106
	v_mul_f32_e32 v107, v1, v107
	v_mul_f32_e32 v108, v2, v108
	v_mul_f32_e32 v109, v3, v109
	v_add_u32_e32 v203, 0x1800000, v12
	global_store_dwordx4 v203, v[102:105], s[86:87] nt
	global_store_dwordx4 v203, v[106:109], s[86:87] offset:16 nt
	v_add_u32_e32 v204, 0xf000, v11
	v_add_u32_e32 v205, 0x1e00000, v10
	global_load_dword v56, v204, s[6:7]
	global_load_dwordx4 v[52:55], v205, s[4:5] nt
	s_waitcnt vmcnt(30)
	v_fmamk_f32 v110, v62, 0x3a800000, v13
	v_mul_f32_e32 v111, 0x4b800000, v110
	v_cmp_gt_f32_e32 vcc, s11, v110
	v_lshlrev_b32_e32 v112, 16, v58
	v_and_b32_e32 v113, 0xffff0000, v58
	v_cndmask_b32_e32 v110, v110, v111, vcc
	v_rsq_f32_e32 v110, v110
	v_lshlrev_b32_e32 v114, 16, v59
	v_mul_f32_e32 v111, 0x45800000, v110
	v_and_b32_e32 v115, 0xffff0000, v59
	v_cndmask_b32_e32 v111, v110, v111, vcc
	v_lshlrev_b32_e32 v116, 16, v60
	v_and_b32_e32 v117, 0xffff0000, v60
	v_lshlrev_b32_e32 v118, 16, v61
	v_and_b32_e32 v119, 0xffff0000, v61
	v_mul_f32_e32 v112, v111, v112
	v_mul_f32_e32 v113, v111, v113
	v_mul_f32_e32 v114, v111, v114
	v_mul_f32_e32 v115, v111, v115
	v_mul_f32_e32 v116, v111, v116
	v_mul_f32_e32 v117, v111, v117
	v_mul_f32_e32 v118, v111, v118
	v_mul_f32_e32 v119, v111, v119
	v_mul_f32_e32 v112, v4, v112
	v_mul_f32_e32 v113, v5, v113
	v_mul_f32_e32 v114, v6, v114
	v_mul_f32_e32 v115, v7, v115
	v_mul_f32_e32 v116, v0, v116
	v_mul_f32_e32 v117, v1, v117
	v_mul_f32_e32 v118, v2, v118
	v_mul_f32_e32 v119, v3, v119
	v_add_u32_e32 v206, 0x1c00000, v12
	global_store_dwordx4 v206, v[112:115], s[86:87] nt
	global_store_dwordx4 v206, v[116:119], s[86:87] offset:16 nt
	v_add_u32_e32 v207, 0x10000, v11
	v_add_u32_e32 v208, 0x2000000, v10
	global_load_dword v62, v207, s[6:7]
	global_load_dwordx4 v[58:61], v208, s[4:5] nt
	s_waitcnt vmcnt(32)
	v_fmamk_f32 v100, v68, 0x3a800000, v13
	v_mul_f32_e32 v101, 0x4b800000, v100
	v_cmp_gt_f32_e32 vcc, s11, v100
	v_lshlrev_b32_e32 v102, 16, v64
	v_and_b32_e32 v103, 0xffff0000, v64
	v_cndmask_b32_e32 v100, v100, v101, vcc
	v_rsq_f32_e32 v100, v100
	v_lshlrev_b32_e32 v104, 16, v65
	v_mul_f32_e32 v101, 0x45800000, v100
	v_and_b32_e32 v105, 0xffff0000, v65
	v_cndmask_b32_e32 v101, v100, v101, vcc
	v_lshlrev_b32_e32 v106, 16, v66
	v_and_b32_e32 v107, 0xffff0000, v66
	v_lshlrev_b32_e32 v108, 16, v67
	v_and_b32_e32 v109, 0xffff0000, v67
	v_mul_f32_e32 v102, v101, v102
	v_mul_f32_e32 v103, v101, v103
	v_mul_f32_e32 v104, v101, v104
	v_mul_f32_e32 v105, v101, v105
	v_mul_f32_e32 v106, v101, v106
	v_mul_f32_e32 v107, v101, v107
	v_mul_f32_e32 v108, v101, v108
	v_mul_f32_e32 v109, v101, v109
	v_mul_f32_e32 v102, v4, v102
	v_mul_f32_e32 v103, v5, v103
	v_mul_f32_e32 v104, v6, v104
	v_mul_f32_e32 v105, v7, v105
	v_mul_f32_e32 v106, v0, v106
	v_mul_f32_e32 v107, v1, v107
	v_mul_f32_e32 v108, v2, v108
	v_mul_f32_e32 v109, v3, v109
	v_add_u32_e32 v209, 0x2000000, v12
	global_store_dwordx4 v209, v[102:105], s[86:87] nt
	global_store_dwordx4 v209, v[106:109], s[86:87] offset:16 nt
	v_add_u32_e32 v210, 0x11000, v11
	v_add_u32_e32 v211, 0x2200000, v10
	global_load_dword v68, v210, s[6:7]
	global_load_dwordx4 v[64:67], v211, s[4:5] nt
	s_waitcnt vmcnt(32)
	v_fmamk_f32 v110, v20, 0x3a800000, v13
	v_mul_f32_e32 v111, 0x4b800000, v110
	v_cmp_gt_f32_e32 vcc, s11, v110
	v_lshlrev_b32_e32 v112, 16, v16
	v_and_b32_e32 v113, 0xffff0000, v16
	v_cndmask_b32_e32 v110, v110, v111, vcc
	v_rsq_f32_e32 v110, v110
	v_lshlrev_b32_e32 v114, 16, v17
	v_mul_f32_e32 v111, 0x45800000, v110
	v_and_b32_e32 v115, 0xffff0000, v17
	v_cndmask_b32_e32 v111, v110, v111, vcc
	v_lshlrev_b32_e32 v116, 16, v18
	v_and_b32_e32 v117, 0xffff0000, v18
	v_lshlrev_b32_e32 v118, 16, v19
	v_and_b32_e32 v119, 0xffff0000, v19
	v_mul_f32_e32 v112, v111, v112
	v_mul_f32_e32 v113, v111, v113
	v_mul_f32_e32 v114, v111, v114
	v_mul_f32_e32 v115, v111, v115
	v_mul_f32_e32 v116, v111, v116
	v_mul_f32_e32 v117, v111, v117
	v_mul_f32_e32 v118, v111, v118
	v_mul_f32_e32 v119, v111, v119
	v_mul_f32_e32 v112, v4, v112
	v_mul_f32_e32 v113, v5, v113
	v_mul_f32_e32 v114, v6, v114
	v_mul_f32_e32 v115, v7, v115
	v_mul_f32_e32 v116, v0, v116
	v_mul_f32_e32 v117, v1, v117
	v_mul_f32_e32 v118, v2, v118
	v_mul_f32_e32 v119, v3, v119
	v_add_u32_e32 v212, 0x2400000, v12
	global_store_dwordx4 v212, v[112:115], s[86:87] nt
	global_store_dwordx4 v212, v[116:119], s[86:87] offset:16 nt
	v_add_u32_e32 v213, 0x12000, v11
	v_add_u32_e32 v214, 0x2400000, v10
	global_load_dword v20, v213, s[6:7]
	global_load_dwordx4 v[16:19], v214, s[4:5] nt
	s_waitcnt vmcnt(32)
	v_fmamk_f32 v100, v26, 0x3a800000, v13
	v_mul_f32_e32 v101, 0x4b800000, v100
	v_cmp_gt_f32_e32 vcc, s11, v100
	v_lshlrev_b32_e32 v102, 16, v22
	v_and_b32_e32 v103, 0xffff0000, v22
	v_cndmask_b32_e32 v100, v100, v101, vcc
	v_rsq_f32_e32 v100, v100
	v_lshlrev_b32_e32 v104, 16, v23
	v_mul_f32_e32 v101, 0x45800000, v100
	v_and_b32_e32 v105, 0xffff0000, v23
	v_cndmask_b32_e32 v101, v100, v101, vcc
	v_lshlrev_b32_e32 v106, 16, v24
	v_and_b32_e32 v107, 0xffff0000, v24
	v_lshlrev_b32_e32 v108, 16, v25
	v_and_b32_e32 v109, 0xffff0000, v25
	v_mul_f32_e32 v102, v101, v102
	v_mul_f32_e32 v103, v101, v103
	v_mul_f32_e32 v104, v101, v104
	v_mul_f32_e32 v105, v101, v105
	v_mul_f32_e32 v106, v101, v106
	v_mul_f32_e32 v107, v101, v107
	v_mul_f32_e32 v108, v101, v108
	v_mul_f32_e32 v109, v101, v109
	v_mul_f32_e32 v102, v4, v102
	v_mul_f32_e32 v103, v5, v103
	v_mul_f32_e32 v104, v6, v104
	v_mul_f32_e32 v105, v7, v105
	v_mul_f32_e32 v106, v0, v106
	v_mul_f32_e32 v107, v1, v107
	v_mul_f32_e32 v108, v2, v108
	v_mul_f32_e32 v109, v3, v109
	v_add_u32_e32 v215, 0x2800000, v12
	global_store_dwordx4 v215, v[102:105], s[86:87] nt
	global_store_dwordx4 v215, v[106:109], s[86:87] offset:16 nt
	v_add_u32_e32 v192, 0x13000, v11
	v_add_u32_e32 v193, 0x2600000, v10
	global_load_dword v26, v192, s[6:7]
	global_load_dwordx4 v[22:25], v193, s[4:5] nt
	s_waitcnt vmcnt(32)
	v_fmamk_f32 v110, v32, 0x3a800000, v13
	v_mul_f32_e32 v111, 0x4b800000, v110
	v_cmp_gt_f32_e32 vcc, s11, v110
	v_lshlrev_b32_e32 v112, 16, v28
	v_and_b32_e32 v113, 0xffff0000, v28
	v_cndmask_b32_e32 v110, v110, v111, vcc
	v_rsq_f32_e32 v110, v110
	v_lshlrev_b32_e32 v114, 16, v29
	v_mul_f32_e32 v111, 0x45800000, v110
	v_and_b32_e32 v115, 0xffff0000, v29
	v_cndmask_b32_e32 v111, v110, v111, vcc
	v_lshlrev_b32_e32 v116, 16, v30
	v_and_b32_e32 v117, 0xffff0000, v30
	v_lshlrev_b32_e32 v118, 16, v31
	v_and_b32_e32 v119, 0xffff0000, v31
	v_mul_f32_e32 v112, v111, v112
	v_mul_f32_e32 v113, v111, v113
	v_mul_f32_e32 v114, v111, v114
	v_mul_f32_e32 v115, v111, v115
	v_mul_f32_e32 v116, v111, v116
	v_mul_f32_e32 v117, v111, v117
	v_mul_f32_e32 v118, v111, v118
	v_mul_f32_e32 v119, v111, v119
	v_mul_f32_e32 v112, v4, v112
	v_mul_f32_e32 v113, v5, v113
	v_mul_f32_e32 v114, v6, v114
	v_mul_f32_e32 v115, v7, v115
	v_mul_f32_e32 v116, v0, v116
	v_mul_f32_e32 v117, v1, v117
	v_mul_f32_e32 v118, v2, v118
	v_mul_f32_e32 v119, v3, v119
	v_add_u32_e32 v194, 0x2c00000, v12
	global_store_dwordx4 v194, v[112:115], s[86:87] nt
	global_store_dwordx4 v194, v[116:119], s[86:87] offset:16 nt
	v_add_u32_e32 v195, 0x14000, v11
	v_add_u32_e32 v196, 0x2800000, v10
	global_load_dword v32, v195, s[6:7]
	global_load_dwordx4 v[28:31], v196, s[4:5] nt
	s_waitcnt vmcnt(32)
	v_fmamk_f32 v100, v38, 0x3a800000, v13
	v_mul_f32_e32 v101, 0x4b800000, v100
	v_cmp_gt_f32_e32 vcc, s11, v100
	v_lshlrev_b32_e32 v102, 16, v34
	v_and_b32_e32 v103, 0xffff0000, v34
	v_cndmask_b32_e32 v100, v100, v101, vcc
	v_rsq_f32_e32 v100, v100
	v_lshlrev_b32_e32 v104, 16, v35
	v_mul_f32_e32 v101, 0x45800000, v100
	v_and_b32_e32 v105, 0xffff0000, v35
	v_cndmask_b32_e32 v101, v100, v101, vcc
	v_lshlrev_b32_e32 v106, 16, v36
	v_and_b32_e32 v107, 0xffff0000, v36
	v_lshlrev_b32_e32 v108, 16, v37
	v_and_b32_e32 v109, 0xffff0000, v37
	v_mul_f32_e32 v102, v101, v102
	v_mul_f32_e32 v103, v101, v103
	v_mul_f32_e32 v104, v101, v104
	v_mul_f32_e32 v105, v101, v105
	v_mul_f32_e32 v106, v101, v106
	v_mul_f32_e32 v107, v101, v107
	v_mul_f32_e32 v108, v101, v108
	v_mul_f32_e32 v109, v101, v109
	v_mul_f32_e32 v102, v4, v102
	v_mul_f32_e32 v103, v5, v103
	v_mul_f32_e32 v104, v6, v104
	v_mul_f32_e32 v105, v7, v105
	v_mul_f32_e32 v106, v0, v106
	v_mul_f32_e32 v107, v1, v107
	v_mul_f32_e32 v108, v2, v108
	v_mul_f32_e32 v109, v3, v109
	v_add_u32_e32 v197, 0x3000000, v12
	global_store_dwordx4 v197, v[102:105], s[86:87] nt
	global_store_dwordx4 v197, v[106:109], s[86:87] offset:16 nt
	v_add_u32_e32 v198, 0x15000, v11
	v_add_u32_e32 v199, 0x2a00000, v10
	global_load_dword v38, v198, s[6:7]
	global_load_dwordx4 v[34:37], v199, s[4:5] nt
	s_waitcnt vmcnt(32)
	v_fmamk_f32 v110, v44, 0x3a800000, v13
	v_mul_f32_e32 v111, 0x4b800000, v110
	v_cmp_gt_f32_e32 vcc, s11, v110
	v_lshlrev_b32_e32 v112, 16, v40
	v_and_b32_e32 v113, 0xffff0000, v40
	v_cndmask_b32_e32 v110, v110, v111, vcc
	v_rsq_f32_e32 v110, v110
	v_lshlrev_b32_e32 v114, 16, v41
	v_mul_f32_e32 v111, 0x45800000, v110
	v_and_b32_e32 v115, 0xffff0000, v41
	v_cndmask_b32_e32 v111, v110, v111, vcc
	v_lshlrev_b32_e32 v116, 16, v42
	v_and_b32_e32 v117, 0xffff0000, v42
	v_lshlrev_b32_e32 v118, 16, v43
	v_and_b32_e32 v119, 0xffff0000, v43
	v_mul_f32_e32 v112, v111, v112
	v_mul_f32_e32 v113, v111, v113
	v_mul_f32_e32 v114, v111, v114
	v_mul_f32_e32 v115, v111, v115
	v_mul_f32_e32 v116, v111, v116
	v_mul_f32_e32 v117, v111, v117
	v_mul_f32_e32 v118, v111, v118
	v_mul_f32_e32 v119, v111, v119
	v_mul_f32_e32 v112, v4, v112
	v_mul_f32_e32 v113, v5, v113
	v_mul_f32_e32 v114, v6, v114
	v_mul_f32_e32 v115, v7, v115
	v_mul_f32_e32 v116, v0, v116
	v_mul_f32_e32 v117, v1, v117
	v_mul_f32_e32 v118, v2, v118
	v_mul_f32_e32 v119, v3, v119
	v_add_u32_e32 v200, 0x3400000, v12
	global_store_dwordx4 v200, v[112:115], s[86:87] nt
	global_store_dwordx4 v200, v[116:119], s[86:87] offset:16 nt
	v_add_u32_e32 v201, 0x16000, v11
	v_add_u32_e32 v202, 0x2c00000, v10
	global_load_dword v44, v201, s[6:7]
	global_load_dwordx4 v[40:43], v202, s[4:5] nt
	s_waitcnt vmcnt(32)
	v_fmamk_f32 v100, v50, 0x3a800000, v13
	v_mul_f32_e32 v101, 0x4b800000, v100
	v_cmp_gt_f32_e32 vcc, s11, v100
	v_lshlrev_b32_e32 v102, 16, v46
	v_and_b32_e32 v103, 0xffff0000, v46
	v_cndmask_b32_e32 v100, v100, v101, vcc
	v_rsq_f32_e32 v100, v100
	v_lshlrev_b32_e32 v104, 16, v47
	v_mul_f32_e32 v101, 0x45800000, v100
	v_and_b32_e32 v105, 0xffff0000, v47
	v_cndmask_b32_e32 v101, v100, v101, vcc
	v_lshlrev_b32_e32 v106, 16, v48
	v_and_b32_e32 v107, 0xffff0000, v48
	v_lshlrev_b32_e32 v108, 16, v49
	v_and_b32_e32 v109, 0xffff0000, v49
	v_mul_f32_e32 v102, v101, v102
	v_mul_f32_e32 v103, v101, v103
	v_mul_f32_e32 v104, v101, v104
	v_mul_f32_e32 v105, v101, v105
	v_mul_f32_e32 v106, v101, v106
	v_mul_f32_e32 v107, v101, v107
	v_mul_f32_e32 v108, v101, v108
	v_mul_f32_e32 v109, v101, v109
	v_mul_f32_e32 v102, v4, v102
	v_mul_f32_e32 v103, v5, v103
	v_mul_f32_e32 v104, v6, v104
	v_mul_f32_e32 v105, v7, v105
	v_mul_f32_e32 v106, v0, v106
	v_mul_f32_e32 v107, v1, v107
	v_mul_f32_e32 v108, v2, v108
	v_mul_f32_e32 v109, v3, v109
	v_add_u32_e32 v203, 0x3800000, v12
	global_store_dwordx4 v203, v[102:105], s[86:87] nt
	global_store_dwordx4 v203, v[106:109], s[86:87] offset:16 nt
	v_add_u32_e32 v204, 0x17000, v11
	v_add_u32_e32 v205, 0x2e00000, v10
	global_load_dword v50, v204, s[6:7]
	global_load_dwordx4 v[46:49], v205, s[4:5] nt
	s_waitcnt vmcnt(32)
	v_fmamk_f32 v110, v56, 0x3a800000, v13
	v_mul_f32_e32 v111, 0x4b800000, v110
	v_cmp_gt_f32_e32 vcc, s11, v110
	v_lshlrev_b32_e32 v112, 16, v52
	v_and_b32_e32 v113, 0xffff0000, v52
	v_cndmask_b32_e32 v110, v110, v111, vcc
	v_rsq_f32_e32 v110, v110
	v_lshlrev_b32_e32 v114, 16, v53
	v_mul_f32_e32 v111, 0x45800000, v110
	v_and_b32_e32 v115, 0xffff0000, v53
	v_cndmask_b32_e32 v111, v110, v111, vcc
	v_lshlrev_b32_e32 v116, 16, v54
	v_and_b32_e32 v117, 0xffff0000, v54
	v_lshlrev_b32_e32 v118, 16, v55
	v_and_b32_e32 v119, 0xffff0000, v55
	v_mul_f32_e32 v112, v111, v112
	v_mul_f32_e32 v113, v111, v113
	v_mul_f32_e32 v114, v111, v114
	v_mul_f32_e32 v115, v111, v115
	v_mul_f32_e32 v116, v111, v116
	v_mul_f32_e32 v117, v111, v117
	v_mul_f32_e32 v118, v111, v118
	v_mul_f32_e32 v119, v111, v119
	v_mul_f32_e32 v112, v4, v112
	v_mul_f32_e32 v113, v5, v113
	v_mul_f32_e32 v114, v6, v114
	v_mul_f32_e32 v115, v7, v115
	v_mul_f32_e32 v116, v0, v116
	v_mul_f32_e32 v117, v1, v117
	v_mul_f32_e32 v118, v2, v118
	v_mul_f32_e32 v119, v3, v119
	v_add_u32_e32 v206, 0x3c00000, v12
	global_store_dwordx4 v206, v[112:115], s[86:87] nt
	global_store_dwordx4 v206, v[116:119], s[86:87] offset:16 nt
	v_add_u32_e32 v207, 0x18000, v11
	v_add_u32_e32 v208, 0x3000000, v10
	global_load_dword v56, v207, s[6:7]
	global_load_dwordx4 v[52:55], v208, s[4:5] nt
	s_waitcnt vmcnt(32)
	v_fmamk_f32 v100, v62, 0x3a800000, v13
	v_mul_f32_e32 v101, 0x4b800000, v100
	v_cmp_gt_f32_e32 vcc, s11, v100
	v_lshlrev_b32_e32 v102, 16, v58
	v_and_b32_e32 v103, 0xffff0000, v58
	v_cndmask_b32_e32 v100, v100, v101, vcc
	v_rsq_f32_e32 v100, v100
	v_lshlrev_b32_e32 v104, 16, v59
	v_mul_f32_e32 v101, 0x45800000, v100
	v_and_b32_e32 v105, 0xffff0000, v59
	v_cndmask_b32_e32 v101, v100, v101, vcc
	v_lshlrev_b32_e32 v106, 16, v60
	v_and_b32_e32 v107, 0xffff0000, v60
	v_lshlrev_b32_e32 v108, 16, v61
	v_and_b32_e32 v109, 0xffff0000, v61
	v_mul_f32_e32 v102, v101, v102
	v_mul_f32_e32 v103, v101, v103
	v_mul_f32_e32 v104, v101, v104
	v_mul_f32_e32 v105, v101, v105
	v_mul_f32_e32 v106, v101, v106
	v_mul_f32_e32 v107, v101, v107
	v_mul_f32_e32 v108, v101, v108
	v_mul_f32_e32 v109, v101, v109
	v_mul_f32_e32 v102, v4, v102
	v_mul_f32_e32 v103, v5, v103
	v_mul_f32_e32 v104, v6, v104
	v_mul_f32_e32 v105, v7, v105
	v_mul_f32_e32 v106, v0, v106
	v_mul_f32_e32 v107, v1, v107
	v_mul_f32_e32 v108, v2, v108
	v_mul_f32_e32 v109, v3, v109
	v_add_u32_e32 v209, 0x4000000, v12
	global_store_dwordx4 v209, v[102:105], s[86:87] nt
	global_store_dwordx4 v209, v[106:109], s[86:87] offset:16 nt
	v_add_u32_e32 v210, 0x19000, v11
	v_add_u32_e32 v211, 0x3200000, v10
	global_load_dword v62, v210, s[6:7]
	global_load_dwordx4 v[58:61], v211, s[4:5] nt
	s_waitcnt vmcnt(32)
	v_fmamk_f32 v110, v68, 0x3a800000, v13
	v_mul_f32_e32 v111, 0x4b800000, v110
	v_cmp_gt_f32_e32 vcc, s11, v110
	v_lshlrev_b32_e32 v112, 16, v64
	v_and_b32_e32 v113, 0xffff0000, v64
	v_cndmask_b32_e32 v110, v110, v111, vcc
	v_rsq_f32_e32 v110, v110
	v_lshlrev_b32_e32 v114, 16, v65
	v_mul_f32_e32 v111, 0x45800000, v110
	v_and_b32_e32 v115, 0xffff0000, v65
	v_cndmask_b32_e32 v111, v110, v111, vcc
	v_lshlrev_b32_e32 v116, 16, v66
	v_and_b32_e32 v117, 0xffff0000, v66
	v_lshlrev_b32_e32 v118, 16, v67
	v_and_b32_e32 v119, 0xffff0000, v67
	v_mul_f32_e32 v112, v111, v112
	v_mul_f32_e32 v113, v111, v113
	v_mul_f32_e32 v114, v111, v114
	v_mul_f32_e32 v115, v111, v115
	v_mul_f32_e32 v116, v111, v116
	v_mul_f32_e32 v117, v111, v117
	v_mul_f32_e32 v118, v111, v118
	v_mul_f32_e32 v119, v111, v119
	v_mul_f32_e32 v112, v4, v112
	v_mul_f32_e32 v113, v5, v113
	v_mul_f32_e32 v114, v6, v114
	v_mul_f32_e32 v115, v7, v115
	v_mul_f32_e32 v116, v0, v116
	v_mul_f32_e32 v117, v1, v117
	v_mul_f32_e32 v118, v2, v118
	v_mul_f32_e32 v119, v3, v119
	v_add_u32_e32 v212, 0x4400000, v12
	global_store_dwordx4 v212, v[112:115], s[86:87] nt
	global_store_dwordx4 v212, v[116:119], s[86:87] offset:16 nt
	v_add_u32_e32 v213, 0x1a000, v11
	v_add_u32_e32 v214, 0x3400000, v10
	global_load_dword v68, v213, s[6:7]
	global_load_dwordx4 v[64:67], v214, s[4:5] nt
	s_waitcnt vmcnt(32)
	v_fmamk_f32 v100, v20, 0x3a800000, v13
	v_mul_f32_e32 v101, 0x4b800000, v100
	v_cmp_gt_f32_e32 vcc, s11, v100
	v_lshlrev_b32_e32 v102, 16, v16
	v_and_b32_e32 v103, 0xffff0000, v16
	v_cndmask_b32_e32 v100, v100, v101, vcc
	v_rsq_f32_e32 v100, v100
	v_lshlrev_b32_e32 v104, 16, v17
	v_mul_f32_e32 v101, 0x45800000, v100
	v_and_b32_e32 v105, 0xffff0000, v17
	v_cndmask_b32_e32 v101, v100, v101, vcc
	v_lshlrev_b32_e32 v106, 16, v18
	v_and_b32_e32 v107, 0xffff0000, v18
	v_lshlrev_b32_e32 v108, 16, v19
	v_and_b32_e32 v109, 0xffff0000, v19
	v_mul_f32_e32 v102, v101, v102
	v_mul_f32_e32 v103, v101, v103
	v_mul_f32_e32 v104, v101, v104
	v_mul_f32_e32 v105, v101, v105
	v_mul_f32_e32 v106, v101, v106
	v_mul_f32_e32 v107, v101, v107
	v_mul_f32_e32 v108, v101, v108
	v_mul_f32_e32 v109, v101, v109
	v_mul_f32_e32 v102, v4, v102
	v_mul_f32_e32 v103, v5, v103
	v_mul_f32_e32 v104, v6, v104
	v_mul_f32_e32 v105, v7, v105
	v_mul_f32_e32 v106, v0, v106
	v_mul_f32_e32 v107, v1, v107
	v_mul_f32_e32 v108, v2, v108
	v_mul_f32_e32 v109, v3, v109
	v_add_u32_e32 v215, 0x4800000, v12
	global_store_dwordx4 v215, v[102:105], s[86:87] nt
	global_store_dwordx4 v215, v[106:109], s[86:87] offset:16 nt
	v_add_u32_e32 v192, 0x1b000, v11
	v_add_u32_e32 v193, 0x3600000, v10
	global_load_dword v20, v192, s[6:7]
	global_load_dwordx4 v[16:19], v193, s[4:5] nt
	s_waitcnt vmcnt(32)
	v_fmamk_f32 v110, v26, 0x3a800000, v13
	v_mul_f32_e32 v111, 0x4b800000, v110
	v_cmp_gt_f32_e32 vcc, s11, v110
	v_lshlrev_b32_e32 v112, 16, v22
	v_and_b32_e32 v113, 0xffff0000, v22
	v_cndmask_b32_e32 v110, v110, v111, vcc
	v_rsq_f32_e32 v110, v110
	v_lshlrev_b32_e32 v114, 16, v23
	v_mul_f32_e32 v111, 0x45800000, v110
	v_and_b32_e32 v115, 0xffff0000, v23
	v_cndmask_b32_e32 v111, v110, v111, vcc
	v_lshlrev_b32_e32 v116, 16, v24
	v_and_b32_e32 v117, 0xffff0000, v24
	v_lshlrev_b32_e32 v118, 16, v25
	v_and_b32_e32 v119, 0xffff0000, v25
	v_mul_f32_e32 v112, v111, v112
	v_mul_f32_e32 v113, v111, v113
	v_mul_f32_e32 v114, v111, v114
	v_mul_f32_e32 v115, v111, v115
	v_mul_f32_e32 v116, v111, v116
	v_mul_f32_e32 v117, v111, v117
	v_mul_f32_e32 v118, v111, v118
	v_mul_f32_e32 v119, v111, v119
	v_mul_f32_e32 v112, v4, v112
	v_mul_f32_e32 v113, v5, v113
	v_mul_f32_e32 v114, v6, v114
	v_mul_f32_e32 v115, v7, v115
	v_mul_f32_e32 v116, v0, v116
	v_mul_f32_e32 v117, v1, v117
	v_mul_f32_e32 v118, v2, v118
	v_mul_f32_e32 v119, v3, v119
	v_add_u32_e32 v194, 0x4c00000, v12
	global_store_dwordx4 v194, v[112:115], s[86:87] nt
	global_store_dwordx4 v194, v[116:119], s[86:87] offset:16 nt
	v_add_u32_e32 v195, 0x1c000, v11
	v_add_u32_e32 v196, 0x3800000, v10
	global_load_dword v26, v195, s[6:7]
	global_load_dwordx4 v[22:25], v196, s[4:5] nt
	s_waitcnt vmcnt(32)
	v_fmamk_f32 v100, v32, 0x3a800000, v13
	v_mul_f32_e32 v101, 0x4b800000, v100
	v_cmp_gt_f32_e32 vcc, s11, v100
	v_lshlrev_b32_e32 v102, 16, v28
	v_and_b32_e32 v103, 0xffff0000, v28
	v_cndmask_b32_e32 v100, v100, v101, vcc
	v_rsq_f32_e32 v100, v100
	v_lshlrev_b32_e32 v104, 16, v29
	v_mul_f32_e32 v101, 0x45800000, v100
	v_and_b32_e32 v105, 0xffff0000, v29
	v_cndmask_b32_e32 v101, v100, v101, vcc
	v_lshlrev_b32_e32 v106, 16, v30
	v_and_b32_e32 v107, 0xffff0000, v30
	v_lshlrev_b32_e32 v108, 16, v31
	v_and_b32_e32 v109, 0xffff0000, v31
	v_mul_f32_e32 v102, v101, v102
	v_mul_f32_e32 v103, v101, v103
	v_mul_f32_e32 v104, v101, v104
	v_mul_f32_e32 v105, v101, v105
	v_mul_f32_e32 v106, v101, v106
	v_mul_f32_e32 v107, v101, v107
	v_mul_f32_e32 v108, v101, v108
	v_mul_f32_e32 v109, v101, v109
	v_mul_f32_e32 v102, v4, v102
	v_mul_f32_e32 v103, v5, v103
	v_mul_f32_e32 v104, v6, v104
	v_mul_f32_e32 v105, v7, v105
	v_mul_f32_e32 v106, v0, v106
	v_mul_f32_e32 v107, v1, v107
	v_mul_f32_e32 v108, v2, v108
	v_mul_f32_e32 v109, v3, v109
	v_add_u32_e32 v197, 0x5000000, v12
	global_store_dwordx4 v197, v[102:105], s[86:87] nt
	global_store_dwordx4 v197, v[106:109], s[86:87] offset:16 nt
	v_add_u32_e32 v198, 0x1d000, v11
	v_add_u32_e32 v199, 0x3a00000, v10
	global_load_dword v32, v198, s[6:7]
	global_load_dwordx4 v[28:31], v199, s[4:5] nt
	s_waitcnt vmcnt(32)
	v_fmamk_f32 v110, v38, 0x3a800000, v13
	v_mul_f32_e32 v111, 0x4b800000, v110
	v_cmp_gt_f32_e32 vcc, s11, v110
	v_lshlrev_b32_e32 v112, 16, v34
	v_and_b32_e32 v113, 0xffff0000, v34
	v_cndmask_b32_e32 v110, v110, v111, vcc
	v_rsq_f32_e32 v110, v110
	v_lshlrev_b32_e32 v114, 16, v35
	v_mul_f32_e32 v111, 0x45800000, v110
	v_and_b32_e32 v115, 0xffff0000, v35
	v_cndmask_b32_e32 v111, v110, v111, vcc
	v_lshlrev_b32_e32 v116, 16, v36
	v_and_b32_e32 v117, 0xffff0000, v36
	v_lshlrev_b32_e32 v118, 16, v37
	v_and_b32_e32 v119, 0xffff0000, v37
	v_mul_f32_e32 v112, v111, v112
	v_mul_f32_e32 v113, v111, v113
	v_mul_f32_e32 v114, v111, v114
	v_mul_f32_e32 v115, v111, v115
	v_mul_f32_e32 v116, v111, v116
	v_mul_f32_e32 v117, v111, v117
	v_mul_f32_e32 v118, v111, v118
	v_mul_f32_e32 v119, v111, v119
	v_mul_f32_e32 v112, v4, v112
	v_mul_f32_e32 v113, v5, v113
	v_mul_f32_e32 v114, v6, v114
	v_mul_f32_e32 v115, v7, v115
	v_mul_f32_e32 v116, v0, v116
	v_mul_f32_e32 v117, v1, v117
	v_mul_f32_e32 v118, v2, v118
	v_mul_f32_e32 v119, v3, v119
	v_add_u32_e32 v200, 0x5400000, v12
	global_store_dwordx4 v200, v[112:115], s[86:87] nt
	global_store_dwordx4 v200, v[116:119], s[86:87] offset:16 nt
	v_add_u32_e32 v201, 0x1e000, v11
	v_add_u32_e32 v202, 0x3c00000, v10
	global_load_dword v38, v201, s[6:7]
	global_load_dwordx4 v[34:37], v202, s[4:5] nt
	s_waitcnt vmcnt(32)
	v_fmamk_f32 v100, v44, 0x3a800000, v13
	v_mul_f32_e32 v101, 0x4b800000, v100
	v_cmp_gt_f32_e32 vcc, s11, v100
	v_lshlrev_b32_e32 v102, 16, v40
	v_and_b32_e32 v103, 0xffff0000, v40
	v_cndmask_b32_e32 v100, v100, v101, vcc
	v_rsq_f32_e32 v100, v100
	v_lshlrev_b32_e32 v104, 16, v41
	v_mul_f32_e32 v101, 0x45800000, v100
	v_and_b32_e32 v105, 0xffff0000, v41
	v_cndmask_b32_e32 v101, v100, v101, vcc
	v_lshlrev_b32_e32 v106, 16, v42
	v_and_b32_e32 v107, 0xffff0000, v42
	v_lshlrev_b32_e32 v108, 16, v43
	v_and_b32_e32 v109, 0xffff0000, v43
	v_mul_f32_e32 v102, v101, v102
	v_mul_f32_e32 v103, v101, v103
	v_mul_f32_e32 v104, v101, v104
	v_mul_f32_e32 v105, v101, v105
	v_mul_f32_e32 v106, v101, v106
	v_mul_f32_e32 v107, v101, v107
	v_mul_f32_e32 v108, v101, v108
	v_mul_f32_e32 v109, v101, v109
	v_mul_f32_e32 v102, v4, v102
	v_mul_f32_e32 v103, v5, v103
	v_mul_f32_e32 v104, v6, v104
	v_mul_f32_e32 v105, v7, v105
	v_mul_f32_e32 v106, v0, v106
	v_mul_f32_e32 v107, v1, v107
	v_mul_f32_e32 v108, v2, v108
	v_mul_f32_e32 v109, v3, v109
	v_add_u32_e32 v203, 0x5800000, v12
	global_store_dwordx4 v203, v[102:105], s[86:87] nt
	global_store_dwordx4 v203, v[106:109], s[86:87] offset:16 nt
	v_add_u32_e32 v204, 0x1f000, v11
	v_add_u32_e32 v205, 0x3e00000, v10
	global_load_dword v44, v204, s[6:7]
	global_load_dwordx4 v[40:43], v205, s[4:5] nt
	s_waitcnt vmcnt(32)
	v_fmamk_f32 v110, v50, 0x3a800000, v13
	v_mul_f32_e32 v111, 0x4b800000, v110
	v_cmp_gt_f32_e32 vcc, s11, v110
	v_lshlrev_b32_e32 v112, 16, v46
	v_and_b32_e32 v113, 0xffff0000, v46
	v_cndmask_b32_e32 v110, v110, v111, vcc
	v_rsq_f32_e32 v110, v110
	v_lshlrev_b32_e32 v114, 16, v47
	v_mul_f32_e32 v111, 0x45800000, v110
	v_and_b32_e32 v115, 0xffff0000, v47
	v_cndmask_b32_e32 v111, v110, v111, vcc
	v_lshlrev_b32_e32 v116, 16, v48
	v_and_b32_e32 v117, 0xffff0000, v48
	v_lshlrev_b32_e32 v118, 16, v49
	v_and_b32_e32 v119, 0xffff0000, v49
	v_mul_f32_e32 v112, v111, v112
	v_mul_f32_e32 v113, v111, v113
	v_mul_f32_e32 v114, v111, v114
	v_mul_f32_e32 v115, v111, v115
	v_mul_f32_e32 v116, v111, v116
	v_mul_f32_e32 v117, v111, v117
	v_mul_f32_e32 v118, v111, v118
	v_mul_f32_e32 v119, v111, v119
	v_mul_f32_e32 v112, v4, v112
	v_mul_f32_e32 v113, v5, v113
	v_mul_f32_e32 v114, v6, v114
	v_mul_f32_e32 v115, v7, v115
	v_mul_f32_e32 v116, v0, v116
	v_mul_f32_e32 v117, v1, v117
	v_mul_f32_e32 v118, v2, v118
	v_mul_f32_e32 v119, v3, v119
	v_add_u32_e32 v206, 0x5c00000, v12
	global_store_dwordx4 v206, v[112:115], s[86:87] nt
	global_store_dwordx4 v206, v[116:119], s[86:87] offset:16 nt
	s_waitcnt vmcnt(30)
	v_fmamk_f32 v100, v56, 0x3a800000, v13
	v_mul_f32_e32 v101, 0x4b800000, v100
	v_cmp_gt_f32_e32 vcc, s11, v100
	v_lshlrev_b32_e32 v102, 16, v52
	v_and_b32_e32 v103, 0xffff0000, v52
	v_cndmask_b32_e32 v100, v100, v101, vcc
	v_rsq_f32_e32 v100, v100
	v_lshlrev_b32_e32 v104, 16, v53
	v_mul_f32_e32 v101, 0x45800000, v100
	v_and_b32_e32 v105, 0xffff0000, v53
	v_cndmask_b32_e32 v101, v100, v101, vcc
	v_lshlrev_b32_e32 v106, 16, v54
	v_and_b32_e32 v107, 0xffff0000, v54
	v_lshlrev_b32_e32 v108, 16, v55
	v_and_b32_e32 v109, 0xffff0000, v55
	v_mul_f32_e32 v102, v101, v102
	v_mul_f32_e32 v103, v101, v103
	v_mul_f32_e32 v104, v101, v104
	v_mul_f32_e32 v105, v101, v105
	v_mul_f32_e32 v106, v101, v106
	v_mul_f32_e32 v107, v101, v107
	v_mul_f32_e32 v108, v101, v108
	v_mul_f32_e32 v109, v101, v109
	v_mul_f32_e32 v102, v4, v102
	v_mul_f32_e32 v103, v5, v103
	v_mul_f32_e32 v104, v6, v104
	v_mul_f32_e32 v105, v7, v105
	v_mul_f32_e32 v106, v0, v106
	v_mul_f32_e32 v107, v1, v107
	v_mul_f32_e32 v108, v2, v108
	v_mul_f32_e32 v109, v3, v109
	v_add_u32_e32 v207, 0x6000000, v12
	global_store_dwordx4 v207, v[102:105], s[86:87] nt
	global_store_dwordx4 v207, v[106:109], s[86:87] offset:16 nt
	s_waitcnt vmcnt(28)
	v_fmamk_f32 v110, v62, 0x3a800000, v13
	v_mul_f32_e32 v111, 0x4b800000, v110
	v_cmp_gt_f32_e32 vcc, s11, v110
	v_lshlrev_b32_e32 v112, 16, v58
	v_and_b32_e32 v113, 0xffff0000, v58
	v_cndmask_b32_e32 v110, v110, v111, vcc
	v_rsq_f32_e32 v110, v110
	v_lshlrev_b32_e32 v114, 16, v59
	v_mul_f32_e32 v111, 0x45800000, v110
	v_and_b32_e32 v115, 0xffff0000, v59
	v_cndmask_b32_e32 v111, v110, v111, vcc
	v_lshlrev_b32_e32 v116, 16, v60
	v_and_b32_e32 v117, 0xffff0000, v60
	v_lshlrev_b32_e32 v118, 16, v61
	v_and_b32_e32 v119, 0xffff0000, v61
	v_mul_f32_e32 v112, v111, v112
	v_mul_f32_e32 v113, v111, v113
	v_mul_f32_e32 v114, v111, v114
	v_mul_f32_e32 v115, v111, v115
	v_mul_f32_e32 v116, v111, v116
	v_mul_f32_e32 v117, v111, v117
	v_mul_f32_e32 v118, v111, v118
	v_mul_f32_e32 v119, v111, v119
	v_mul_f32_e32 v112, v4, v112
	v_mul_f32_e32 v113, v5, v113
	v_mul_f32_e32 v114, v6, v114
	v_mul_f32_e32 v115, v7, v115
	v_mul_f32_e32 v116, v0, v116
	v_mul_f32_e32 v117, v1, v117
	v_mul_f32_e32 v118, v2, v118
	v_mul_f32_e32 v119, v3, v119
	v_add_u32_e32 v208, 0x6400000, v12
	global_store_dwordx4 v208, v[112:115], s[86:87] nt
	global_store_dwordx4 v208, v[116:119], s[86:87] offset:16 nt
	s_waitcnt vmcnt(26)
	v_fmamk_f32 v100, v68, 0x3a800000, v13
	v_mul_f32_e32 v101, 0x4b800000, v100
	v_cmp_gt_f32_e32 vcc, s11, v100
	v_lshlrev_b32_e32 v102, 16, v64
	v_and_b32_e32 v103, 0xffff0000, v64
	v_cndmask_b32_e32 v100, v100, v101, vcc
	v_rsq_f32_e32 v100, v100
	v_lshlrev_b32_e32 v104, 16, v65
	v_mul_f32_e32 v101, 0x45800000, v100
	v_and_b32_e32 v105, 0xffff0000, v65
	v_cndmask_b32_e32 v101, v100, v101, vcc
	v_lshlrev_b32_e32 v106, 16, v66
	v_and_b32_e32 v107, 0xffff0000, v66
	v_lshlrev_b32_e32 v108, 16, v67
	v_and_b32_e32 v109, 0xffff0000, v67
	v_mul_f32_e32 v102, v101, v102
	v_mul_f32_e32 v103, v101, v103
	v_mul_f32_e32 v104, v101, v104
	v_mul_f32_e32 v105, v101, v105
	v_mul_f32_e32 v106, v101, v106
	v_mul_f32_e32 v107, v101, v107
	v_mul_f32_e32 v108, v101, v108
	v_mul_f32_e32 v109, v101, v109
	v_mul_f32_e32 v102, v4, v102
	v_mul_f32_e32 v103, v5, v103
	v_mul_f32_e32 v104, v6, v104
	v_mul_f32_e32 v105, v7, v105
	v_mul_f32_e32 v106, v0, v106
	v_mul_f32_e32 v107, v1, v107
	v_mul_f32_e32 v108, v2, v108
	v_mul_f32_e32 v109, v3, v109
	v_add_u32_e32 v209, 0x6800000, v12
	global_store_dwordx4 v209, v[102:105], s[86:87] nt
	global_store_dwordx4 v209, v[106:109], s[86:87] offset:16 nt
	s_waitcnt vmcnt(24)
	v_fmamk_f32 v110, v20, 0x3a800000, v13
	v_mul_f32_e32 v111, 0x4b800000, v110
	v_cmp_gt_f32_e32 vcc, s11, v110
	v_lshlrev_b32_e32 v112, 16, v16
	v_and_b32_e32 v113, 0xffff0000, v16
	v_cndmask_b32_e32 v110, v110, v111, vcc
	v_rsq_f32_e32 v110, v110
	v_lshlrev_b32_e32 v114, 16, v17
	v_mul_f32_e32 v111, 0x45800000, v110
	v_and_b32_e32 v115, 0xffff0000, v17
	v_cndmask_b32_e32 v111, v110, v111, vcc
	v_lshlrev_b32_e32 v116, 16, v18
	v_and_b32_e32 v117, 0xffff0000, v18
	v_lshlrev_b32_e32 v118, 16, v19
	v_and_b32_e32 v119, 0xffff0000, v19
	v_mul_f32_e32 v112, v111, v112
	v_mul_f32_e32 v113, v111, v113
	v_mul_f32_e32 v114, v111, v114
	v_mul_f32_e32 v115, v111, v115
	v_mul_f32_e32 v116, v111, v116
	v_mul_f32_e32 v117, v111, v117
	v_mul_f32_e32 v118, v111, v118
	v_mul_f32_e32 v119, v111, v119
	v_mul_f32_e32 v112, v4, v112
	v_mul_f32_e32 v113, v5, v113
	v_mul_f32_e32 v114, v6, v114
	v_mul_f32_e32 v115, v7, v115
	v_mul_f32_e32 v116, v0, v116
	v_mul_f32_e32 v117, v1, v117
	v_mul_f32_e32 v118, v2, v118
	v_mul_f32_e32 v119, v3, v119
	v_add_u32_e32 v210, 0x6c00000, v12
	global_store_dwordx4 v210, v[112:115], s[86:87] nt
	global_store_dwordx4 v210, v[116:119], s[86:87] offset:16 nt
	s_waitcnt vmcnt(22)
	v_fmamk_f32 v100, v26, 0x3a800000, v13
	v_mul_f32_e32 v101, 0x4b800000, v100
	v_cmp_gt_f32_e32 vcc, s11, v100
	v_lshlrev_b32_e32 v102, 16, v22
	v_and_b32_e32 v103, 0xffff0000, v22
	v_cndmask_b32_e32 v100, v100, v101, vcc
	v_rsq_f32_e32 v100, v100
	v_lshlrev_b32_e32 v104, 16, v23
	v_mul_f32_e32 v101, 0x45800000, v100
	v_and_b32_e32 v105, 0xffff0000, v23
	v_cndmask_b32_e32 v101, v100, v101, vcc
	v_lshlrev_b32_e32 v106, 16, v24
	v_and_b32_e32 v107, 0xffff0000, v24
	v_lshlrev_b32_e32 v108, 16, v25
	v_and_b32_e32 v109, 0xffff0000, v25
	v_mul_f32_e32 v102, v101, v102
	v_mul_f32_e32 v103, v101, v103
	v_mul_f32_e32 v104, v101, v104
	v_mul_f32_e32 v105, v101, v105
	v_mul_f32_e32 v106, v101, v106
	v_mul_f32_e32 v107, v101, v107
	v_mul_f32_e32 v108, v101, v108
	v_mul_f32_e32 v109, v101, v109
	v_mul_f32_e32 v102, v4, v102
	v_mul_f32_e32 v103, v5, v103
	v_mul_f32_e32 v104, v6, v104
	v_mul_f32_e32 v105, v7, v105
	v_mul_f32_e32 v106, v0, v106
	v_mul_f32_e32 v107, v1, v107
	v_mul_f32_e32 v108, v2, v108
	v_mul_f32_e32 v109, v3, v109
	v_add_u32_e32 v211, 0x7000000, v12
	global_store_dwordx4 v211, v[102:105], s[86:87] nt
	global_store_dwordx4 v211, v[106:109], s[86:87] offset:16 nt
	s_waitcnt vmcnt(20)
	v_fmamk_f32 v110, v32, 0x3a800000, v13
	v_mul_f32_e32 v111, 0x4b800000, v110
	v_cmp_gt_f32_e32 vcc, s11, v110
	v_lshlrev_b32_e32 v112, 16, v28
	v_and_b32_e32 v113, 0xffff0000, v28
	v_cndmask_b32_e32 v110, v110, v111, vcc
	v_rsq_f32_e32 v110, v110
	v_lshlrev_b32_e32 v114, 16, v29
	v_mul_f32_e32 v111, 0x45800000, v110
	v_and_b32_e32 v115, 0xffff0000, v29
	v_cndmask_b32_e32 v111, v110, v111, vcc
	v_lshlrev_b32_e32 v116, 16, v30
	v_and_b32_e32 v117, 0xffff0000, v30
	v_lshlrev_b32_e32 v118, 16, v31
	v_and_b32_e32 v119, 0xffff0000, v31
	v_mul_f32_e32 v112, v111, v112
	v_mul_f32_e32 v113, v111, v113
	v_mul_f32_e32 v114, v111, v114
	v_mul_f32_e32 v115, v111, v115
	v_mul_f32_e32 v116, v111, v116
	v_mul_f32_e32 v117, v111, v117
	v_mul_f32_e32 v118, v111, v118
	v_mul_f32_e32 v119, v111, v119
	v_mul_f32_e32 v112, v4, v112
	v_mul_f32_e32 v113, v5, v113
	v_mul_f32_e32 v114, v6, v114
	v_mul_f32_e32 v115, v7, v115
	v_mul_f32_e32 v116, v0, v116
	v_mul_f32_e32 v117, v1, v117
	v_mul_f32_e32 v118, v2, v118
	v_mul_f32_e32 v119, v3, v119
	v_add_u32_e32 v212, 0x7400000, v12
	global_store_dwordx4 v212, v[112:115], s[86:87] nt
	global_store_dwordx4 v212, v[116:119], s[86:87] offset:16 nt
	s_waitcnt vmcnt(18)
	v_fmamk_f32 v100, v38, 0x3a800000, v13
	v_mul_f32_e32 v101, 0x4b800000, v100
	v_cmp_gt_f32_e32 vcc, s11, v100
	v_lshlrev_b32_e32 v102, 16, v34
	v_and_b32_e32 v103, 0xffff0000, v34
	v_cndmask_b32_e32 v100, v100, v101, vcc
	v_rsq_f32_e32 v100, v100
	v_lshlrev_b32_e32 v104, 16, v35
	v_mul_f32_e32 v101, 0x45800000, v100
	v_and_b32_e32 v105, 0xffff0000, v35
	v_cndmask_b32_e32 v101, v100, v101, vcc
	v_lshlrev_b32_e32 v106, 16, v36
	v_and_b32_e32 v107, 0xffff0000, v36
	v_lshlrev_b32_e32 v108, 16, v37
	v_and_b32_e32 v109, 0xffff0000, v37
	v_mul_f32_e32 v102, v101, v102
	v_mul_f32_e32 v103, v101, v103
	v_mul_f32_e32 v104, v101, v104
	v_mul_f32_e32 v105, v101, v105
	v_mul_f32_e32 v106, v101, v106
	v_mul_f32_e32 v107, v101, v107
	v_mul_f32_e32 v108, v101, v108
	v_mul_f32_e32 v109, v101, v109
	v_mul_f32_e32 v102, v4, v102
	v_mul_f32_e32 v103, v5, v103
	v_mul_f32_e32 v104, v6, v104
	v_mul_f32_e32 v105, v7, v105
	v_mul_f32_e32 v106, v0, v106
	v_mul_f32_e32 v107, v1, v107
	v_mul_f32_e32 v108, v2, v108
	v_mul_f32_e32 v109, v3, v109
	v_add_u32_e32 v213, 0x7800000, v12
	global_store_dwordx4 v213, v[102:105], s[86:87] nt
	global_store_dwordx4 v213, v[106:109], s[86:87] offset:16 nt
	s_waitcnt vmcnt(16)
	v_fmamk_f32 v110, v44, 0x3a800000, v13
	v_mul_f32_e32 v111, 0x4b800000, v110
	v_cmp_gt_f32_e32 vcc, s11, v110
	v_lshlrev_b32_e32 v112, 16, v40
	v_and_b32_e32 v113, 0xffff0000, v40
	v_cndmask_b32_e32 v110, v110, v111, vcc
	v_rsq_f32_e32 v110, v110
	v_lshlrev_b32_e32 v114, 16, v41
	v_mul_f32_e32 v111, 0x45800000, v110
	v_and_b32_e32 v115, 0xffff0000, v41
	v_cndmask_b32_e32 v111, v110, v111, vcc
	v_lshlrev_b32_e32 v116, 16, v42
	v_and_b32_e32 v117, 0xffff0000, v42
	v_lshlrev_b32_e32 v118, 16, v43
	v_and_b32_e32 v119, 0xffff0000, v43
	v_mul_f32_e32 v112, v111, v112
	v_mul_f32_e32 v113, v111, v113
	v_mul_f32_e32 v114, v111, v114
	v_mul_f32_e32 v115, v111, v115
	v_mul_f32_e32 v116, v111, v116
	v_mul_f32_e32 v117, v111, v117
	v_mul_f32_e32 v118, v111, v118
	v_mul_f32_e32 v119, v111, v119
	v_mul_f32_e32 v112, v4, v112
	v_mul_f32_e32 v113, v5, v113
	v_mul_f32_e32 v114, v6, v114
	v_mul_f32_e32 v115, v7, v115
	v_mul_f32_e32 v116, v0, v116
	v_mul_f32_e32 v117, v1, v117
	v_mul_f32_e32 v118, v2, v118
	v_mul_f32_e32 v119, v3, v119
	v_add_u32_e32 v214, 0x7c00000, v12
	global_store_dwordx4 v214, v[112:115], s[86:87] nt
	global_store_dwordx4 v214, v[116:119], s[86:87] offset:16 nt
